# U-pass expert blocks regrouped by 4 (no hazard nops, saddr loads); K swizzle on NA/window/ctx units
# speedup vs baseline: 1.0371x; 1.0027x over previous
.LBB0_609:
	s_or_b64 exec, exec, s[0:1]
	s_lshl_b32 s19, s7, 2
	s_max_i32 s0, s19, 4
	s_lshl_b32 s2, s7, 8
	s_add_i32 s0, s0, -4
	s_min_u32 s12, s0, 0xf4
	s_ashr_i32 s3, s2, 31
	s_lshl_b32 s13, s12, 6
	s_mul_i32 s7, s7, 0x240000
	v_writelane_b32 v255, s2, 10
	s_mul_hi_i32 s0, s2, 0x2400
	v_ashrrev_i32_e32 v18, 4, v48
	v_writelane_b32 v255, s3, 11
	s_add_u32 s2, s34, s7
	s_addc_u32 s3, s35, s0
	s_lshl_b32 s0, s6, 7
	s_ashr_i32 s1, s0, 31
	s_lshl_b64 s[4:5], s[0:1], 1
	s_add_u32 s0, s2, s4
	s_addc_u32 s1, s3, s5
	v_readlane_b32 s2, v254, 51
	s_add_u32 s14, s2, s4
	v_readlane_b32 s2, v254, 52
	s_addc_u32 s15, s2, s5
	v_readlane_b32 s2, v254, 53
	s_add_u32 s16, s2, s4
	v_readlane_b32 s2, v254, 54
	v_writelane_b32 v255, s4, 12
	s_addc_u32 s17, s2, s5
	s_add_i32 s20, 0, 0x10000
	s_cmp_lg_u32 0, -1
	s_mul_i32 s2, s12, 0x90000
	v_lshlrev_b32_e32 v19, 3, v48
	s_cselect_b32 s21, 0, 0
	s_add_u32 s36, s14, s2
	v_and_b32_e32 v20, 0x78, v19
	v_mul_lo_u32 v0, v18, s68
	s_addc_u32 s37, s15, 0
	v_or_b32_e32 v0, v0, v20
	s_add_u32 s42, s16, s2
	v_lshlrev_b32_e32 v192, 1, v0
	s_addc_u32 s43, s17, 0
	s_waitcnt lgkmcnt(0)
	s_barrier
	v_add_u32_e32 v150, 0x48000, v192
	global_load_dwordx4 v[0:3], v192, s[42:43]
	global_load_dwordx4 v[4:7], v150, s[42:43]
	global_load_dwordx4 v[8:11], v192, s[36:37]
	global_load_dwordx4 v[12:15], v150, s[36:37]
	v_ashrrev_i32_e32 v49, 1, v48
	v_bfe_u32 v154, v48, 5, 1
	v_bfi_b32 v21, s67, v49, v48
	v_mov_b64_e32 v[16:17], s[0:1]
	v_mad_i64_i32 v[16:17], s[0:1], v21, s66, v[16:17]
	v_lshlrev_b32_e32 v148, 4, v154
	v_mov_b32_e32 v149, v193
	v_lshl_add_u64 v[16:17], v[16:17], 0, v[148:149]
	global_load_dwordx4 v[100:103], v[16:17], off
	global_load_dwordx4 v[104:107], v[16:17], off offset:32
	global_load_dwordx4 v[120:123], v[16:17], off offset:64
	global_load_dwordx4 v[124:127], v[16:17], off offset:96
	global_load_dwordx4 v[116:119], v[16:17], off offset:128
	global_load_dwordx4 v[112:115], v[16:17], off offset:160
	global_load_dwordx4 v[108:111], v[16:17], off offset:192
	global_load_dwordx4 v[96:99], v[16:17], off offset:224
	v_and_b32_e32 v22, 0xfffff0, v18
	v_lshlrev_b32_e32 v23, 1, v18
	v_lshrrev_b32_e32 v24, 1, v18
	v_and_b32_e32 v25, 3, v18
	v_add_u32_e32 v26, 32, v18
	v_and_or_b32 v22, v23, 8, v22
	v_and_or_b32 v23, v24, 4, v25
	v_and_b32_e32 v24, 0xfffff0, v26
	v_lshlrev_b32_e32 v25, 1, v26
	v_and_b32_e32 v21, 0xf0, v48
	v_bfe_u32 v19, v19, 5, 2
	v_lshlrev_b32_e32 v18, 8, v18
	v_lshlrev_b32_e32 v20, 1, v20
	v_lshlrev_b32_e32 v26, 8, v26
	v_lshrrev_b32_e32 v22, 1, v22
	v_and_or_b32 v24, v25, 8, v24
	v_and_b32_e32 v27, 48, v20
	v_bitop3_b32 v18, v20, v18, v21 bitop3:0xde
	v_bitop3_b32 v20, v20, v26, v21 bitop3:0xde
	v_or_b32_e32 v21, v22, v19
	v_lshrrev_b32_e32 v22, 1, v24
	v_lshlrev_b32_e32 v23, 6, v23
	v_add_u32_e32 v153, 0, v18
	v_lshlrev_b32_e32 v18, 9, v21
	v_or_b32_e32 v19, v22, v19
	v_and_b32_e32 v149, 31, v48
	v_lshlrev_b32_e32 v50, 4, v48
	v_or3_b32 v18, v18, v23, v27
	v_lshlrev_b32_e32 v19, 9, v19
	v_lshlrev_b32_e32 v40, 8, v149
	v_or3_b32 v19, v19, v23, v27
	v_add_u32_e32 v156, 0, v18
	v_and_b32_e32 v41, 0xf0, v50
	v_add_u32_e32 v155, 0, v20
	v_add_u32_e32 v157, 0, v19
	s_waitcnt vmcnt(0)
	v_or_b32_e32 v36, 64, v148
	v_bitop3_b32 v36, v36, v40, v41 bitop3:0xde
	v_add_u32_e32 v162, 0, v36
	v_or_b32_e32 v36, 0x60, v148
	v_bitop3_b32 v36, v36, v40, v41 bitop3:0xde
	s_waitcnt vmcnt(11)
	ds_write_b128 v156, v[0:3]
	s_waitcnt vmcnt(10)
	ds_write_b128 v157, v[4:7]
	s_waitcnt vmcnt(9)
	ds_write_b128 v153, v[8:11] offset:32768
	s_waitcnt vmcnt(8)
	ds_write_b128 v155, v[12:15] offset:32768
	v_bitop3_b32 v0, v148, v40, v41 bitop3:0xde
	v_add_u32_e32 v158, 0, v0
	s_waitcnt lgkmcnt(0)
	s_barrier
	ds_read_b128 v[0:3], v158 offset:32768
	v_or_b32_e32 v4, 32, v148
	v_bitop3_b32 v32, v4, v40, v41 bitop3:0xde
	v_add_u32_e32 v161, 0, v32
	ds_read_b128 v[32:35], v161 offset:32768
	s_waitcnt vmcnt(7) lgkmcnt(1)
	v_mfma_f32_32x32x16_bf16 v[16:31], v[0:3], v[100:103], 0
	ds_read_b128 v[0:3], v158 offset:40960
	v_add_u32_e32 v160, 0, v36
	v_or_b32_e32 v36, 0x80, v148
	v_bitop3_b32 v36, v36, v40, v41 bitop3:0xde
	v_add_u32_e32 v166, 0, v36
	ds_read_b128 v[36:39], v166 offset:32768
	v_or_b32_e32 v43, 0xc0, v148
	s_waitcnt vmcnt(6) lgkmcnt(2)
	v_mfma_f32_32x32x16_bf16 v[16:31], v[32:35], v[104:107], v[16:31]
	ds_read_b128 v[32:35], v161 offset:40960
	v_ashrrev_i32_e32 v51, 7, v48
	v_add_u32_e32 v42, s19, v51
	v_max_i32_e32 v44, 4, v42
	v_and_or_b32 v168, v49, 32, v149
	v_sub_u32_e64 v45, v168, 8 clamp
	v_min_u32_e32 v54, 48, v45
	s_waitcnt lgkmcnt(2)
	v_mfma_f32_32x32x16_bf16 v[0:15], v[0:3], v[100:103], 0
	v_lshlrev_b32_e32 v173, 2, v154
	v_writelane_b32 v255, s5, 13
	v_or_b32_e32 v174, 1, v173
	v_sub_u32_e32 v52, s12, v42
	v_max_i32_e32 v52, -7, v52
	v_or_b32_e32 v175, 2, v173
	v_add_u32_e32 v52, 7, v52
	s_waitcnt lgkmcnt(0)
	v_mfma_f32_32x32x16_bf16 v[0:15], v[32:35], v[104:107], v[0:15]
	ds_read_b128 v[32:35], v162 offset:32768
	v_cmp_ge_u32_e64 s[2:3], v175, v54
	v_min_u32_e32 v52, 14, v52
	v_or_b32_e32 v176, 3, v173
	v_mul_u32_u24_e32 v52, 31, v52
	v_cmp_ge_u32_e64 s[4:5], v176, v54
	v_sub_u32_e32 v52, v52, v168
	s_waitcnt vmcnt(5) lgkmcnt(0)
	v_mfma_f32_32x32x16_bf16 v[16:31], v[32:35], v[120:123], v[16:31]
	ds_read_b128 v[32:35], v162 offset:40960
	v_or_b32_e32 v177, 8, v173
	v_add_u32_e32 v52, 15, v52
	v_cmp_ge_u32_e64 s[6:7], v177, v54
	v_add_u32_e32 v53, v52, v173
	v_or_b32_e32 v178, 9, v173
	s_add_i32 s18, 0, 0x11000
	s_waitcnt lgkmcnt(0)
	v_mfma_f32_32x32x16_bf16 v[0:15], v[32:35], v[120:123], v[0:15]
	ds_read_b128 v[32:35], v160 offset:32768
	v_cmp_ge_u32_e64 s[8:9], v178, v54
	v_or_b32_e32 v179, 10, v173
	v_cmp_ge_u32_e64 s[22:23], v179, v54
	v_or_b32_e32 v180, 11, v173
	v_add_u32_e32 v60, v52, v178
	v_add_u32_e32 v61, v52, v179
	s_waitcnt vmcnt(4) lgkmcnt(0)
	v_mfma_f32_32x32x16_bf16 v[16:31], v[32:35], v[124:127], v[16:31]
	ds_read_b128 v[32:35], v160 offset:40960
	v_add_u32_e32 v62, v52, v180
	v_or_b32_e32 v181, 16, v173
	v_or_b32_e32 v182, 17, v173
	v_or_b32_e32 v183, 18, v173
	v_or_b32_e32 v184, 19, v173
	v_or_b32_e32 v185, 24, v173
	s_waitcnt lgkmcnt(0)
	v_mfma_f32_32x32x16_bf16 v[0:15], v[32:35], v[124:127], v[0:15]
	v_or_b32_e32 v32, 0xa0, v148
	v_bitop3_b32 v32, v32, v40, v41 bitop3:0xde
	v_add_u32_e32 v165, 0, v32
	ds_read_b128 v[32:35], v165 offset:32768
	v_or_b32_e32 v186, 25, v173
	v_cmp_ge_u32_e64 s[34:35], v186, v54
	v_or_b32_e32 v187, 26, v173
	s_waitcnt vmcnt(3)
	v_mfma_f32_32x32x16_bf16 v[16:31], v[36:39], v[116:119], v[16:31]
	v_bitop3_b32 v37, v43, v40, v41 bitop3:0xde
	v_or_b32_e32 v36, 0xe0, v148
	v_add_u32_e32 v164, 0, v37
	v_bitop3_b32 v40, v36, v40, v41 bitop3:0xde
	ds_read_b128 v[36:39], v164 offset:32768
	v_add_u32_e32 v163, 0, v40
	ds_read_b128 v[56:59], v163 offset:32768
	s_waitcnt vmcnt(2) lgkmcnt(2)
	v_mfma_f32_32x32x16_bf16 v[16:31], v[32:35], v[112:115], v[16:31]
	v_add_u32_e32 v32, -4, v44
	v_min_u32_e32 v169, 0xf8, v32
	v_add_u32_e32 v170, 8, v169
	v_cmp_ge_u32_e32 vcc, s12, v32
	v_cmp_lt_u32_e64 s[0:1], s12, v170
	s_and_b64 s[10:11], vcc, s[0:1]
	v_cmp_ge_u32_e64 s[0:1], v173, v54
	s_waitcnt vmcnt(1) lgkmcnt(1)
	v_mfma_f32_32x32x16_bf16 v[16:31], v[36:39], v[108:111], v[16:31]
	ds_read_b128 v[44:47], v166 offset:40960
	ds_read_b128 v[40:43], v165 offset:40960
	ds_read_b128 v[32:35], v164 offset:40960
	ds_read_b128 v[36:39], v163 offset:40960
	v_writelane_b32 v255, s0, 14
	s_and_b64 vcc, s[0:1], s[10:11]
	v_cndmask_b32_e32 v53, 0, v53, vcc
	v_writelane_b32 v255, s1, 15
	v_cmp_ge_u32_e64 s[0:1], v174, v54
	v_lshl_add_u32 v55, v53, 2, s18
	s_waitcnt vmcnt(0) lgkmcnt(4)
	v_mfma_f32_32x32x16_bf16 v[16:31], v[56:59], v[96:99], v[16:31]
	v_writelane_b32 v255, s0, 16
	v_add_u32_e32 v53, v52, v174
	v_add_u32_e32 v59, v52, v177
	v_writelane_b32 v255, s1, 17
	v_writelane_b32 v255, s2, 18
	s_and_b64 s[0:1], s[0:1], s[10:11]
	v_cndmask_b32_e64 v53, 0, v53, s[0:1]
	v_writelane_b32 v255, s3, 19
	v_writelane_b32 v255, s4, 20
	v_lshl_add_u32 v56, v53, 2, s18
	v_add_u32_e32 v53, v52, v175
	v_writelane_b32 v255, s5, 21
	v_writelane_b32 v255, s6, 22
	s_and_b64 s[2:3], s[2:3], s[10:11]
	v_cndmask_b32_e64 v53, 0, v53, s[2:3]
	v_writelane_b32 v255, s7, 23
	v_writelane_b32 v255, s8, 24
	v_lshl_add_u32 v57, v53, 2, s18
	v_add_u32_e32 v53, v52, v176
	v_writelane_b32 v255, s9, 25
	v_writelane_b32 v255, s22, 26
	s_and_b64 s[38:39], s[10:11], s[22:23]
	s_and_b64 s[4:5], s[4:5], s[10:11]
	v_writelane_b32 v255, s23, 27
	v_cmp_ge_u32_e64 s[22:23], v180, v54
	s_and_b64 s[6:7], s[10:11], s[6:7]
	s_and_b64 s[8:9], s[10:11], s[8:9]
	s_and_b64 s[40:41], s[10:11], s[22:23]
	v_cndmask_b32_e64 v53, 0, v53, s[4:5]
	v_cndmask_b32_e64 v59, 0, v59, s[6:7]
	v_cndmask_b32_e64 v60, 0, v60, s[8:9]
	v_cndmask_b32_e64 v61, 0, v61, s[38:39]
	v_cndmask_b32_e64 v62, 0, v62, s[40:41]
	v_lshl_add_u32 v58, v53, 2, s18
	v_lshl_add_u32 v59, v59, 2, s18
	v_lshl_add_u32 v60, v60, 2, s18
	v_lshl_add_u32 v61, v61, 2, s18
	v_lshl_add_u32 v62, v62, 2, s18
	ds_read_b32 v55, v55
	ds_read_b32 v56, v56
	ds_read_b32 v57, v57
	ds_read_b32 v58, v58
	ds_read_b32 v59, v59
	ds_read_b32 v60, v60
	ds_read_b32 v61, v61
	ds_read_b32 v62, v62
	s_waitcnt lgkmcnt(6)
	v_add_f32_e32 v17, v17, v56
	v_cndmask_b32_e64 v17, v217, v17, s[0:1]
	v_cmp_ge_u32_e64 s[0:1], v181, v54
	s_waitcnt lgkmcnt(5)
	v_add_f32_e32 v18, v18, v57
	v_cndmask_b32_e64 v18, v217, v18, s[2:3]
	v_writelane_b32 v255, s0, 28
	v_cmp_lt_u32_e64 s[2:3], v173, v54
	v_add_f32_e32 v16, v16, v55
	v_writelane_b32 v255, s1, 29
	s_and_b64 s[0:1], s[10:11], s[0:1]
	v_writelane_b32 v255, s2, 30
	v_cndmask_b32_e32 v16, v217, v16, vcc
	s_and_b64 vcc, s[0:1], s[2:3]
	v_writelane_b32 v255, s3, 31
	v_cmp_ge_u32_e64 s[0:1], v182, v54
	v_add_u32_e32 v53, 16, v54
	v_cmp_lt_u32_e64 s[2:3], v182, v53
	v_writelane_b32 v255, s0, 32
	s_waitcnt lgkmcnt(4)
	v_add_f32_e32 v19, v19, v58
	v_cndmask_b32_e64 v19, v217, v19, s[4:5]
	v_writelane_b32 v255, s1, 33
	s_and_b64 s[0:1], s[10:11], s[0:1]
	v_writelane_b32 v255, s2, 34
	s_and_b64 s[0:1], s[0:1], s[2:3]
	v_cmp_lt_u32_e64 s[4:5], v183, v53
	v_writelane_b32 v255, s3, 35
	v_cmp_ge_u32_e64 s[2:3], v183, v54
	s_waitcnt lgkmcnt(3)
	v_add_f32_e32 v20, v20, v59
	v_cndmask_b32_e64 v20, v217, v20, s[6:7]
	v_writelane_b32 v255, s2, 36
	v_cmp_lt_u32_e64 s[6:7], v184, v53
	v_add_u32_e32 v55, v52, v181
	v_writelane_b32 v255, s3, 37
	s_and_b64 s[2:3], s[10:11], s[2:3]
	v_writelane_b32 v255, s4, 38
	s_and_b64 s[2:3], s[2:3], s[4:5]
	v_add_u32_e32 v56, v52, v182
	v_writelane_b32 v255, s5, 39
	v_cmp_ge_u32_e64 s[4:5], v184, v54
	v_add_u32_e32 v57, v52, v183
	v_add_u32_e32 v58, v52, v184
	v_writelane_b32 v255, s4, 40
	v_cndmask_b32_e32 v55, 0, v55, vcc
	v_cndmask_b32_e64 v56, 0, v56, s[0:1]
	v_writelane_b32 v255, s5, 41
	s_and_b64 s[4:5], s[10:11], s[4:5]
	v_writelane_b32 v255, s6, 42
	s_and_b64 s[4:5], s[4:5], s[6:7]
	v_cndmask_b32_e64 v57, 0, v57, s[2:3]
	v_cndmask_b32_e64 v58, 0, v58, s[4:5]
	v_lshl_add_u32 v55, v55, 2, s18
	v_lshl_add_u32 v56, v56, 2, s18
	v_lshl_add_u32 v57, v57, 2, s18
	v_lshl_add_u32 v58, v58, 2, s18
	v_writelane_b32 v255, s7, 43
	ds_read_b32 v55, v55
	ds_read_b32 v56, v56
	ds_read_b32 v57, v57
	ds_read_b32 v58, v58
	v_cmp_ge_u32_e64 s[6:7], v185, v54
	s_waitcnt lgkmcnt(3)
	v_add_f32_e32 v24, v24, v55
	v_cmp_lt_u32_e64 s[30:31], v185, v53
	v_writelane_b32 v255, s6, 44
	v_cndmask_b32_e32 v24, v217, v24, vcc
	v_add_u32_e32 v55, v52, v185
	v_writelane_b32 v255, s7, 45
	s_and_b64 s[6:7], s[10:11], s[6:7]
	s_and_b64 vcc, s[6:7], s[30:31]
	v_cndmask_b32_e32 v55, 0, v55, vcc
	v_lshl_add_u32 v55, v55, 2, s18
	ds_read_b32 v55, v55
	s_waitcnt lgkmcnt(3)
	v_add_f32_e32 v25, v25, v56
	s_waitcnt lgkmcnt(2)
	v_add_f32_e32 v26, v26, v57
	v_cndmask_b32_e64 v25, v217, v25, s[0:1]
	v_cndmask_b32_e64 v26, v217, v26, s[2:3]
	s_and_b64 s[0:1], s[10:11], s[34:35]
	s_waitcnt lgkmcnt(0)
	v_add_f32_e32 v28, v28, v55
	v_cmp_lt_u32_e64 s[2:3], v186, v53
	v_cndmask_b32_e32 v28, v217, v28, vcc
	v_add_u32_e32 v55, v52, v186
	s_and_b64 vcc, s[0:1], s[2:3]
	v_cndmask_b32_e32 v55, 0, v55, vcc
	v_lshl_add_u32 v55, v55, 2, s18
	ds_read_b32 v55, v55
	v_mfma_f32_32x32x16_bf16 v[0:15], v[44:47], v[116:119], v[0:15]
	v_cmp_ge_u32_e64 s[0:1], v187, v54
	s_mov_b64 s[24:25], s[2:3]
	s_mov_b64 s[26:27], s[0:1]
	s_waitcnt lgkmcnt(0)
	v_add_f32_e32 v29, v29, v55
	s_and_b64 s[0:1], s[10:11], s[0:1]
	v_cmp_lt_u32_e64 s[2:3], v187, v53
	v_cndmask_b32_e32 v29, v217, v29, vcc
	v_add_u32_e32 v44, v52, v187
	s_and_b64 vcc, s[0:1], s[2:3]
	v_cndmask_b32_e32 v44, 0, v44, vcc
	v_lshl_add_u32 v44, v44, 2, s18
	v_mfma_f32_32x32x16_bf16 v[0:15], v[40:43], v[112:115], v[0:15]
	ds_read_b32 v44, v44
	v_or_b32_e32 v188, 27, v173
	v_cmp_ge_u32_e64 s[52:53], v188, v54
	s_and_b64 s[0:1], s[10:11], s[52:53]
	v_cmp_lt_u32_e64 s[54:55], v188, v53
	s_waitcnt lgkmcnt(0)
	v_add_f32_e32 v30, v30, v44
	v_cndmask_b32_e32 v30, v217, v30, vcc
	v_add_u32_e32 v40, v52, v188
	s_and_b64 vcc, s[0:1], s[54:55]
	v_cndmask_b32_e32 v40, 0, v40, vcc
	v_mfma_f32_32x32x16_bf16 v[0:15], v[32:35], v[108:111], v[0:15]
	v_lshl_add_u32 v40, v40, 2, s18
	ds_read_b32 v40, v40
	v_or_b32_e32 v189, 32, v173
	v_cmp_ge_u32_e64 s[56:57], v189, v54
	s_and_b64 s[0:1], s[10:11], s[56:57]
	v_cmp_lt_u32_e64 s[58:59], v189, v53
	s_waitcnt lgkmcnt(0)
	v_add_f32_e32 v31, v31, v40
	v_cndmask_b32_e32 v31, v217, v31, vcc
	v_add_u32_e32 v32, v52, v189
	s_and_b64 vcc, s[0:1], s[58:59]
	v_mfma_f32_32x32x16_bf16 v[0:15], v[36:39], v[96:99], v[0:15]
	v_cndmask_b32_e32 v32, 0, v32, vcc
	v_lshl_add_u32 v32, v32, 2, s18
	ds_read_b32 v32, v32
	v_or_b32_e32 v190, 33, v173
	v_cmp_ge_u32_e64 s[60:61], v190, v54
	s_and_b64 s[0:1], s[10:11], s[60:61]
	v_cmp_lt_u32_e64 s[62:63], v190, v53
	s_waitcnt lgkmcnt(0)
	s_nop 3
	v_add_f32_e32 v0, v0, v32
	v_cndmask_b32_e32 v32, v217, v0, vcc
	v_add_u32_e32 v0, v52, v190
	s_and_b64 vcc, s[0:1], s[62:63]
	v_cndmask_b32_e32 v0, 0, v0, vcc
	v_lshl_add_u32 v0, v0, 2, s18
	ds_read_b32 v0, v0
	v_or_b32_e32 v191, 34, v173
	v_cmp_ge_u32_e64 s[64:65], v191, v54
	s_and_b64 s[0:1], s[10:11], s[64:65]
	v_cmp_lt_u32_e64 s[66:67], v191, v53
	s_waitcnt lgkmcnt(0)
	v_add_f32_e32 v0, v1, v0
	v_cndmask_b32_e32 v33, v217, v0, vcc
	v_add_u32_e32 v0, v52, v191
	s_and_b64 vcc, s[0:1], s[66:67]
	v_cndmask_b32_e32 v0, 0, v0, vcc
	v_lshl_add_u32 v0, v0, 2, s18
	ds_read_b32 v0, v0
	v_or_b32_e32 v200, 35, v173
	v_cmp_ge_u32_e64 s[68:69], v200, v54
	s_and_b64 s[0:1], s[10:11], s[68:69]
	v_cmp_lt_u32_e64 s[70:71], v200, v53
	s_waitcnt lgkmcnt(0)
	v_add_f32_e32 v0, v2, v0
	v_cndmask_b32_e32 v34, v217, v0, vcc
	v_add_u32_e32 v0, v52, v200
	s_and_b64 vcc, s[0:1], s[70:71]
	v_cndmask_b32_e32 v0, 0, v0, vcc
	v_lshl_add_u32 v0, v0, 2, s18
	ds_read_b32 v0, v0
	v_or_b32_e32 v201, 40, v173
	v_cmp_ge_u32_e64 s[72:73], v201, v54
	s_and_b64 s[0:1], s[10:11], s[72:73]
	v_cmp_lt_u32_e64 s[74:75], v201, v53
	s_waitcnt lgkmcnt(0)
	v_add_f32_e32 v0, v3, v0
	v_cndmask_b32_e32 v35, v217, v0, vcc
	v_add_u32_e32 v0, v52, v201
	s_and_b64 vcc, s[0:1], s[74:75]
	v_cndmask_b32_e32 v0, 0, v0, vcc
	v_lshl_add_u32 v0, v0, 2, s18
	ds_read_b32 v0, v0
	v_or_b32_e32 v203, 41, v173
	v_cmp_ge_u32_e64 s[76:77], v203, v54
	s_and_b64 s[0:1], s[10:11], s[76:77]
	v_cmp_lt_u32_e64 s[78:79], v203, v53
	s_waitcnt lgkmcnt(0)
	v_add_f32_e32 v0, v4, v0
	v_cndmask_b32_e32 v36, v217, v0, vcc
	v_add_u32_e32 v0, v52, v203
	s_and_b64 vcc, s[0:1], s[78:79]
	v_cndmask_b32_e32 v0, 0, v0, vcc
	v_lshl_add_u32 v0, v0, 2, s18
	ds_read_b32 v0, v0
	v_or_b32_e32 v204, 42, v173
	v_cmp_ge_u32_e64 s[80:81], v204, v54
	s_and_b64 s[0:1], s[10:11], s[80:81]
	v_cmp_lt_u32_e64 s[82:83], v204, v53
	s_waitcnt lgkmcnt(0)
	v_add_f32_e32 v0, v5, v0
	v_cndmask_b32_e32 v37, v217, v0, vcc
	v_add_u32_e32 v0, v52, v204
	s_and_b64 vcc, s[0:1], s[82:83]
	v_cndmask_b32_e32 v0, 0, v0, vcc
	v_lshl_add_u32 v0, v0, 2, s18
	ds_read_b32 v0, v0
	v_or_b32_e32 v205, 43, v173
	v_cmp_ge_u32_e64 s[84:85], v205, v54
	s_and_b64 s[0:1], s[10:11], s[84:85]
	v_cmp_lt_u32_e64 s[86:87], v205, v53
	s_waitcnt lgkmcnt(0)
	v_add_f32_e32 v0, v6, v0
	v_cndmask_b32_e32 v46, v217, v0, vcc
	v_add_u32_e32 v0, v52, v205
	s_and_b64 vcc, s[0:1], s[86:87]
	v_cndmask_b32_e32 v0, 0, v0, vcc
	v_lshl_add_u32 v0, v0, 2, s18
	ds_read_b32 v0, v0
	v_or_b32_e32 v206, 48, v173
	v_cmp_lt_u32_e64 s[88:89], v206, v53
	v_or_b32_e32 v207, 49, v173
	s_waitcnt lgkmcnt(0)
	v_add_f32_e32 v0, v7, v0
	v_cndmask_b32_e32 v47, v217, v0, vcc
	v_add_u32_e32 v0, v52, v206
	s_and_b64 vcc, s[10:11], s[88:89]
	v_cndmask_b32_e32 v0, 0, v0, vcc
	v_lshl_add_u32 v0, v0, 2, s18
	ds_read_b32 v0, v0
	v_cmp_lt_u32_e64 s[90:91], v207, v53
	v_add_f32_e32 v21, v21, v60
	v_or_b32_e32 v208, 50, v173
	v_cmp_lt_u32_e64 s[92:93], v208, v53
	s_waitcnt lgkmcnt(0)
	v_add_f32_e32 v0, v8, v0
	v_cndmask_b32_e32 v60, v217, v0, vcc
	v_add_u32_e32 v0, v52, v207
	s_and_b64 vcc, s[10:11], s[90:91]
	v_cndmask_b32_e32 v0, 0, v0, vcc
	v_lshl_add_u32 v0, v0, 2, s18
	ds_read_b32 v0, v0
	v_add_f32_e32 v22, v22, v61
	v_or_b32_e32 v209, 51, v173
	v_cmp_lt_u32_e64 s[94:95], v209, v53
	v_add_f32_e32 v23, v23, v62
	s_waitcnt lgkmcnt(0)
	v_add_f32_e32 v0, v9, v0
	v_cndmask_b32_e32 v61, v217, v0, vcc
	v_add_u32_e32 v0, v52, v208
	s_and_b64 vcc, s[10:11], s[92:93]
	v_cndmask_b32_e32 v0, 0, v0, vcc
	v_lshl_add_u32 v0, v0, 2, s18
	ds_read_b32 v0, v0
	v_or_b32_e32 v210, 56, v173
	v_cmp_lt_u32_e64 s[96:97], v210, v53
	v_or_b32_e32 v211, 57, v173
	s_mov_b64 s[28:29], s[2:3]
	s_waitcnt lgkmcnt(0)
	v_add_f32_e32 v0, v10, v0
	v_cndmask_b32_e32 v62, v217, v0, vcc
	v_add_u32_e32 v0, v52, v209
	s_and_b64 vcc, s[10:11], s[94:95]
	v_cndmask_b32_e32 v0, 0, v0, vcc
	v_lshl_add_u32 v0, v0, 2, s18
	ds_read_b32 v0, v0
	v_cmp_lt_u32_e64 s[2:3], v211, v53
	v_or_b32_e32 v212, 58, v173
	v_cmp_lt_u32_e64 s[0:1], v212, v53
	s_waitcnt lgkmcnt(0)
	v_add_f32_e32 v0, v11, v0
	v_cndmask_b32_e32 v63, v217, v0, vcc
	v_add_u32_e32 v0, v52, v210
	s_and_b64 vcc, s[10:11], s[96:97]
	v_cndmask_b32_e32 v0, 0, v0, vcc
	v_lshl_add_u32 v0, v0, 2, s18
	ds_read_b32 v0, v0
	v_or_b32_e32 v213, 59, v173
	v_cmp_lt_u32_e64 s[6:7], v213, v53
	v_cndmask_b32_e64 v21, v217, v21, s[8:9]
	v_cndmask_b32_e64 v22, v217, v22, s[38:39]
	s_waitcnt lgkmcnt(0)
	v_add_f32_e32 v0, v12, v0
	v_cndmask_b32_e32 v64, v217, v0, vcc
	v_add_u32_e32 v0, v52, v211
	s_and_b64 vcc, s[10:11], s[2:3]
	v_cndmask_b32_e32 v0, 0, v0, vcc
	v_lshl_add_u32 v0, v0, 2, s18
	ds_read_b32 v0, v0
	v_cndmask_b32_e64 v23, v217, v23, s[40:41]
	v_add_f32_e32 v27, v27, v58
	v_cndmask_b32_e64 v27, v217, v27, s[4:5]
	s_mov_b32 s4, 0x42b504f3
	s_waitcnt lgkmcnt(0)
	v_add_f32_e32 v0, v13, v0
	v_cndmask_b32_e32 v65, v217, v0, vcc
	v_add_u32_e32 v0, v52, v212
	s_and_b64 vcc, s[10:11], s[0:1]
	v_cndmask_b32_e32 v0, 0, v0, vcc
	v_lshl_add_u32 v0, v0, 2, s18
	ds_read_b32 v0, v0
	v_mov_b32_e32 v2, 0xf149f2ca
	v_and_b32_e32 v68, 63, v48
	v_and_b32_e32 v152, 0xffffffe0, v49
	v_mov_b32_e32 v194, 0x8000
	s_waitcnt lgkmcnt(0)
	v_add_f32_e32 v0, v14, v0
	v_cndmask_b32_e32 v66, v217, v0, vcc
	v_add_u32_e32 v0, v52, v213
	s_and_b64 vcc, s[10:11], s[6:7]
	v_cndmask_b32_e32 v0, 0, v0, vcc
	v_lshl_add_u32 v0, v0, 2, s18
	ds_read_b32 v0, v0
	v_mov_b32_e32 v216, 0xc000
	v_mov_b32_e32 v151, v193
	s_waitcnt lgkmcnt(0)
	v_add_f32_e32 v0, v15, v0
	v_cndmask_b32_e32 v67, v217, v0, vcc
	v_max_f32_e32 v0, v16, v17
	v_max3_f32 v0, v0, v18, v19
	v_max3_f32 v0, v0, v20, v21
	v_max3_f32 v0, v0, v22, v23
	v_max3_f32 v0, v0, v24, v25
	v_max3_f32 v0, v0, v26, v27
	v_max3_f32 v0, v0, v28, v29
	v_max3_f32 v0, v0, v30, v31
	v_max3_f32 v0, v0, v32, v33
	v_max3_f32 v0, v0, v34, v35
	v_max3_f32 v0, v0, v36, v37
	v_max3_f32 v0, v0, v46, v47
	v_max3_f32 v0, v0, v60, v61
	v_max3_f32 v0, v0, v62, v63
	v_max3_f32 v0, v0, v64, v65
	v_max3_f32 v0, v0, v66, v67
	v_mov_b32_e32 v1, v0
	s_nop 1
	v_permlane32_swap_b32_e32 v0, v1
	v_max_f32_e32 v1, v1, v1
	v_max_f32_e32 v0, v0, v0
	v_max_f32_e32 v0, v0, v1
	v_add_f32_e32 v1, 0x7149f2ca, v0
	v_cmp_ge_f32_e32 vcc, s4, v1
	s_cmp_eq_u64 vcc, exec
	s_cselect_b64 vcc, -1, 0
	s_add_u32 s4, s36, 0x90000
	s_addc_u32 s5, s37, 0
	s_add_u32 s8, s42, 0x90000
	s_addc_u32 s9, s43, 0
	global_load_dwordx4 v[38:41], v150, s[8:9]
	global_load_dwordx4 v[42:45], v192, s[8:9]
	global_load_dwordx4 v[52:55], v192, s[4:5]
	global_load_dwordx4 v[56:59], v150, s[4:5]
	v_max_f32_e32 v0, 0xf149f2ca, v0
	v_sub_f32_e32 v1, 0xf149f2ca, v0
	v_mul_f32_e32 v1, 0x3e0293ee, v1
	v_exp_f32_e32 v1, v1
	v_cndmask_b32_e32 v222, v0, v2, vcc
	v_and_b32_e32 v0, 0x3fffffc0, v48
	v_lshl_add_u32 v159, v0, 2, s20
	v_cndmask_b32_e64 v214, v1, 1.0, vcc
	v_lshlrev_b32_e32 v0, 3, v68
	v_and_b32_e32 v1, 0xc0, v50
	v_lshlrev_b32_e32 v2, 1, v48
	v_and_or_b32 v1, v0, 24, v1
	v_and_b32_e32 v2, 32, v2
	v_and_b32_e32 v0, 0x100, v0
	v_or3_b32 v0, v1, v2, v0
	v_readlane_b32 s36, v254, 57
	v_add_u32_e32 v202, s21, v0
	s_addk_i32 s21, 0x4000
	v_readlane_b32 s37, v254, 58
	v_add_u32_e32 v167, s21, v0
	v_sub_u32_e32 v0, s12, v51
	s_mov_b32 s5, s37
	v_subrev_u32_e32 v215, s19, v0
	v_readlane_b32 s38, v254, 59
	v_readlane_b32 s39, v254, 60
	v_readlane_b32 s40, v254, 61
	v_readlane_b32 s41, v254, 62
	v_readlane_b32 s42, v254, 63
	v_readlane_b32 s43, v255, 0
	v_readlane_b32 s44, v255, 1
	v_readlane_b32 s45, v255, 2
	v_readlane_b32 s46, v255, 3
	v_readlane_b32 s47, v255, 4
	v_readlane_b32 s48, v255, 5
	v_readlane_b32 s49, v255, 6
	v_readlane_b32 s50, v255, 7
	v_readlane_b32 s51, v255, 8
	v_writelane_b32 v254, s4, 57
	v_mul_f32_e32 v129, 0xbe0293ee, v222
	s_mov_b32 s36, s37
	v_writelane_b32 v255, s11, 0
	v_writelane_b32 v255, s12, 1
	v_writelane_b32 v255, s13, 2
	v_writelane_b32 v255, s14, 3
	v_writelane_b32 v255, s15, 4
	v_writelane_b32 v254, s5, 58
	v_writelane_b32 v255, s16, 5
	v_writelane_b32 v254, s6, 59
	v_writelane_b32 v255, s17, 6
	v_fmamk_f32 v16, v16, 0x3e0293ee, v129
	v_fmamk_f32 v17, v17, 0x3e0293ee, v129
	v_fmamk_f32 v18, v18, 0x3e0293ee, v129
	v_fmamk_f32 v19, v19, 0x3e0293ee, v129
	v_fmamk_f32 v20, v20, 0x3e0293ee, v129
	v_fmamk_f32 v21, v21, 0x3e0293ee, v129
	v_fmamk_f32 v22, v22, 0x3e0293ee, v129
	v_fmamk_f32 v23, v23, 0x3e0293ee, v129
	v_fmamk_f32 v24, v24, 0x3e0293ee, v129
	v_fmamk_f32 v25, v25, 0x3e0293ee, v129
	v_fmamk_f32 v26, v26, 0x3e0293ee, v129
	v_fmamk_f32 v27, v27, 0x3e0293ee, v129
	v_fmamk_f32 v28, v28, 0x3e0293ee, v129
	v_fmamk_f32 v29, v29, 0x3e0293ee, v129
	v_fmamk_f32 v30, v30, 0x3e0293ee, v129
	v_fmamk_f32 v31, v31, 0x3e0293ee, v129
	s_mov_b32 s38, s37
	s_mov_b32 s39, s37
	s_mov_b32 s40, s37
	s_mov_b32 s41, s37
	s_mov_b32 s42, s37
	s_mov_b32 s43, s37
	s_mov_b32 s44, s37
	s_mov_b32 s45, s37
	s_mov_b32 s46, s37
	s_mov_b32 s47, s37
	s_mov_b32 s48, s37
	s_mov_b32 s49, s37
	s_mov_b32 s50, s37
	s_mov_b32 s51, s37
	v_writelane_b32 v254, s7, 60
	v_writelane_b32 v255, s18, 7
	v_mov_b64_e32 v[0:1], s[36:37]
	v_exp_f32_e32 v236, v16
	v_exp_f32_e32 v238, v17
	v_exp_f32_e32 v145, v18
	v_exp_f32_e32 v237, v19
	v_exp_f32_e32 v146, v20
	v_exp_f32_e32 v235, v21
	v_exp_f32_e32 v147, v22
	v_exp_f32_e32 v234, v23
	v_exp_f32_e32 v231, v24
	v_exp_f32_e32 v233, v25
	v_exp_f32_e32 v230, v26
	v_exp_f32_e32 v232, v27
	v_exp_f32_e32 v227, v28
	v_exp_f32_e32 v229, v29
	v_exp_f32_e32 v226, v30
	v_exp_f32_e32 v228, v31
	v_writelane_b32 v254, s8, 61
	v_writelane_b32 v255, s19, 8
	v_mov_b64_e32 v[14:15], s[50:51]
	s_waitcnt vmcnt(0)
	v_writelane_b32 v254, s9, 62
	v_mov_b64_e32 v[2:3], s[38:39]
	v_mov_b64_e32 v[4:5], s[40:41]
	v_mov_b64_e32 v[6:7], s[42:43]
	v_mov_b64_e32 v[8:9], s[44:45]
	v_mov_b64_e32 v[10:11], s[46:47]
	v_mov_b64_e32 v[12:13], s[48:49]
	v_readlane_b32 s48, v255, 26
	v_readlane_b32 s46, v255, 24
	v_readlane_b32 s44, v255, 22
	v_readlane_b32 s42, v255, 20
	v_readlane_b32 s40, v255, 18
	v_readlane_b32 s38, v255, 16
	v_readlane_b32 s36, v255, 14
	v_fmamk_f32 v134, v32, 0x3e0293ee, v129
	v_fmamk_f32 v135, v33, 0x3e0293ee, v129
	v_fmamk_f32 v138, v34, 0x3e0293ee, v129
	v_fmamk_f32 v139, v35, 0x3e0293ee, v129
	v_fmamk_f32 v130, v36, 0x3e0293ee, v129
	v_fmamk_f32 v131, v37, 0x3e0293ee, v129
	v_fmamk_f32 v132, v46, 0x3e0293ee, v129
	v_fmamk_f32 v133, v47, 0x3e0293ee, v129
	v_fmamk_f32 v136, v60, 0x3e0293ee, v129
	v_fmamk_f32 v137, v61, 0x3e0293ee, v129
	v_fmamk_f32 v142, v62, 0x3e0293ee, v129
	v_fmamk_f32 v143, v63, 0x3e0293ee, v129
	s_waitcnt vmcnt(2)
	ds_write_b128 v156, v[42:45] offset:16384
	ds_write_b128 v157, v[38:41] offset:16384
	s_waitcnt vmcnt(1)
	ds_write_b128 v153, v[52:55] offset:49152
	s_waitcnt vmcnt(0)
	ds_write_b128 v155, v[56:59] offset:49152
	v_mov_b64_e32 v[62:63], v[14:15]
	v_mov_b64_e32 v[46:47], v[14:15]
	v_mov_b64_e32 v[30:31], v[14:15]
	v_writelane_b32 v254, s10, 63
	s_mov_b64 s[50:51], s[22:23]
	v_readlane_b32 s49, v255, 27
	v_readlane_b32 s47, v255, 25
	v_readlane_b32 s45, v255, 23
	v_readlane_b32 s43, v255, 21
	v_readlane_b32 s41, v255, 19
	v_readlane_b32 s39, v255, 17
	v_readlane_b32 s37, v255, 15
	v_fmamk_f32 v140, v64, 0x3e0293ee, v129
	v_fmamk_f32 v141, v65, 0x3e0293ee, v129
	v_fmamk_f32 v128, v66, 0x3e0293ee, v129
	v_fmac_f32_e32 v129, 0x3e0293ee, v67
	v_lshl_add_u32 v171, v149, 2, v159
	v_mov_b32_e32 v172, 0
	v_mov_b64_e32 v[60:61], v[12:13]
	v_mov_b64_e32 v[58:59], v[10:11]
	v_mov_b64_e32 v[56:57], v[8:9]
	v_mov_b64_e32 v[54:55], v[6:7]
	v_mov_b64_e32 v[52:53], v[4:5]
	v_mov_b64_e32 v[50:51], v[2:3]
	v_mov_b64_e32 v[48:49], v[0:1]
	v_mov_b64_e32 v[44:45], v[12:13]
	v_mov_b64_e32 v[42:43], v[10:11]
	v_mov_b64_e32 v[40:41], v[8:9]
	v_mov_b64_e32 v[38:39], v[6:7]
	v_mov_b64_e32 v[36:37], v[4:5]
	v_mov_b64_e32 v[34:35], v[2:3]
	v_mov_b64_e32 v[32:33], v[0:1]
	v_mov_b64_e32 v[28:29], v[12:13]
	v_mov_b64_e32 v[26:27], v[10:11]
	v_mov_b64_e32 v[24:25], v[8:9]
	v_mov_b64_e32 v[22:23], v[6:7]
	v_mov_b64_e32 v[20:21], v[4:5]
	v_mov_b64_e32 v[18:19], v[2:3]
	v_mov_b64_e32 v[16:17], v[0:1]
	s_mov_b32 s19, -1
	v_cmp_gt_u32_e64 s[4:5], 32, v68
	s_waitcnt lgkmcnt(0)
	s_barrier

.LBB0_634:
	v_mov_b32_e32 v0, v193
	v_readlane_b32 s0, v254, 6
	v_mbcnt_lo_u32_b32 v0, -1, v0
	v_mbcnt_hi_u32_b32 v0, -1, v0
	v_add_u32_e32 v33, s0, v0
	s_ashr_i32 s0, s18, 31
	s_lshr_b32 s0, s0, 30
	s_add_i32 s1, s18, s0
	s_and_b32 s0, s1, -4
	s_lshl_b32 s1, s1, 6
	s_and_b32 s4, s1, 0xffffff00
	s_max_i32 s5, s4, 0x80
	s_min_i32 s1, s4, 0x3e80
	s_sub_i32 s2, s1, s5
	s_sub_i32 s0, s18, s0
	s_add_i32 s1, s2, 0x200
	s_ashr_i32 s20, s1, 6
	s_ashr_i32 s1, s0, 31
	s_add_i32 s19, s5, 0xffffff80
	s_lshl_b64 s[6:7], s[0:1], 2
	s_add_u32 s6, s12, s6
	s_addc_u32 s7, s13, s7
	s_mul_i32 s3, s4, 0x2400
	s_mul_hi_i32 s1, s4, 0x2400
	s_add_u32 s3, s34, s3
	global_load_dword v149, v193, s[6:7]
	s_addc_u32 s1, s35, s1
	s_lshl_b32 s6, s0, 7
	s_ashr_i32 s7, s6, 31
	s_lshl_b64 s[6:7], s[6:7], 1
	s_add_u32 s3, s3, s6
	s_addc_u32 s1, s1, s7
	s_add_u32 s8, s3, 0x1c00
	s_addc_u32 s9, s1, 0
	s_bfe_u32 s1, s0, 0x10007
	s_add_i32 s0, s0, s1
	s_bfe_i32 s0, s0, 0x80000
	s_sext_i32_i16 s0, s0
	s_lshl_b32 s0, s0, 6
	s_and_b32 s0, s0, 0xffffff80
	s_ashr_i32 s1, s0, 31
	s_lshl_b64 s[0:1], s[0:1], 1
	s_add_u32 s21, s14, s0
	s_addc_u32 s22, s15, s1
	v_ashrrev_i32_e32 v0, 1, v33
	s_add_u32 s23, s16, s0
	v_bfe_u32 v155, v33, 5, 1
	v_and_b32_e32 v148, 0xffffffe0, v0
	v_bfi_b32 v2, s67, v0, v33
	v_mov_b64_e32 v[0:1], s[8:9]
	s_addc_u32 s24, s17, s1
	v_mad_i64_i32 v[0:1], s[0:1], v2, s66, v[0:1]
	v_lshlrev_b32_e32 v150, 4, v155
	v_mov_b32_e32 v151, v193
	v_ashrrev_i32_e32 v16, 4, v33
	v_lshl_add_u64 v[0:1], v[0:1], 0, v[150:151]
	v_and_b32_e32 v2, 0xfffff0, v16
	v_lshlrev_b32_e32 v3, 1, v16
	global_load_dwordx4 v[124:127], v[0:1], off
	global_load_dwordx4 v[120:123], v[0:1], off offset:32
	global_load_dwordx4 v[116:119], v[0:1], off offset:64
	global_load_dwordx4 v[112:115], v[0:1], off offset:96
	global_load_dwordx4 v[108:111], v[0:1], off offset:128
	global_load_dwordx4 v[104:107], v[0:1], off offset:160
	global_load_dwordx4 v[100:103], v[0:1], off offset:192
	global_load_dwordx4 v[96:99], v[0:1], off offset:224
	v_lshlrev_b32_e32 v0, 3, v33
	v_and_or_b32 v2, v3, 8, v2
	v_and_b32_e32 v1, 0x78, v0
	v_lshrrev_b32_e32 v3, 1, v16
	v_lshrrev_b32_e32 v2, 1, v2
	v_bfe_u32 v0, v0, 5, 2
	v_and_b32_e32 v4, 3, v16
	v_or_b32_e32 v2, v2, v0
	v_and_or_b32 v3, v3, 4, v4
	v_lshlrev_b32_e32 v17, 1, v1
	v_lshlrev_b32_e32 v2, 9, v2
	v_lshlrev_b32_e32 v3, 6, v3
	v_and_b32_e32 v4, 48, v17
	v_add_u32_e32 v19, 32, v16
	s_min_i32 s0, s20, 0
	v_or3_b32 v18, v2, v3, v4
	v_and_b32_e32 v2, 0xfffff0, v19
	v_lshlrev_b32_e32 v5, 1, v19
	s_cmp_gt_i32 s20, 0
	v_and_or_b32 v2, v5, 8, v2
	s_cselect_b32 s1, s19, 0x4000
	s_lshl_b32 s0, s0, 6
	v_lshrrev_b32_e32 v2, 1, v2
	s_sub_i32 s0, s1, s0
	v_or_b32_e32 v0, v2, v0
	s_mul_i32 s3, s0, 0x2400
	v_lshlrev_b32_e32 v0, 9, v0
	s_add_u32 s0, s21, s3
	v_or3_b32 v20, v0, v3, v4
	v_mul_lo_u32 v0, v16, s68
	s_addc_u32 s1, s22, 0
	v_or_b32_e32 v0, v0, v1
	s_add_u32 s8, s23, s3
	v_lshlrev_b32_e32 v192, 1, v0
	s_addc_u32 s9, s24, 0
	v_add_u32_e32 v152, 0x48000, v192
	global_load_dwordx4 v[0:3], v192, s[8:9]
	global_load_dwordx4 v[4:7], v152, s[8:9]
	global_load_dwordx4 v[8:11], v192, s[0:1]
	global_load_dwordx4 v[12:15], v152, s[0:1]
	v_add_u32_e32 v169, 0, v18
	s_waitcnt vmcnt(0)
	v_and_b32_e32 v154, 31, v33
	v_lshlrev_b32_e32 v32, 8, v154
	v_add_u32_e32 v170, 0, v20
	v_or_b32_e32 v34, 32, v150
	s_cmp_lt_i32 s20, 1
	s_waitcnt vmcnt(3)
	ds_write_b128 v169, v[0:3]
	v_lshlrev_b32_e32 v0, 8, v16
	v_and_b32_e32 v1, 0xf0, v33
	v_bitop3_b32 v0, v17, v0, v1 bitop3:0xde
	v_add_u32_e32 v171, 0, v0
	v_lshlrev_b32_e32 v0, 8, v19
	v_bitop3_b32 v0, v17, v0, v1 bitop3:0xde
	v_add_u32_e32 v172, 0, v0
	v_lshlrev_b32_e32 v0, 4, v33
	v_and_b32_e32 v42, 0xf0, v0
	v_bitop3_b32 v0, v150, v32, v42 bitop3:0xde
	v_add_u32_e32 v166, 0, v0
	s_waitcnt vmcnt(2)
	ds_write_b128 v170, v[4:7]
	s_waitcnt vmcnt(1)
	ds_write_b128 v171, v[8:11] offset:32768
	s_waitcnt vmcnt(0)
	ds_write_b128 v172, v[12:15] offset:32768
	s_waitcnt lgkmcnt(0)
	s_barrier
	ds_read_b128 v[0:3], v166 offset:32768
	ds_read_b128 v[4:7], v166 offset:40960
	s_waitcnt lgkmcnt(1)
	v_mfma_f32_32x32x16_bf16 v[16:31], v[0:3], v[124:127], 0
	v_bitop3_b32 v34, v34, v32, v42 bitop3:0xde
	v_add_u32_e32 v168, 0, v34
	ds_read_b128 v[34:37], v168 offset:32768
	ds_read_b128 v[38:41], v168 offset:40960
	s_waitcnt lgkmcnt(2)
	v_mfma_f32_32x32x16_bf16 v[0:15], v[4:7], v[124:127], 0
	s_waitcnt lgkmcnt(1)
	v_mfma_f32_32x32x16_bf16 v[16:31], v[34:37], v[120:123], v[16:31]
	v_or_b32_e32 v34, 64, v150
	v_bitop3_b32 v34, v34, v32, v42 bitop3:0xde
	v_add_u32_e32 v167, 0, v34
	s_waitcnt lgkmcnt(0)
	v_mfma_f32_32x32x16_bf16 v[0:15], v[38:41], v[120:123], v[0:15]
	ds_read_b128 v[34:37], v167 offset:32768
	ds_read_b128 v[38:41], v167 offset:40960
	s_waitcnt lgkmcnt(1)
	v_mfma_f32_32x32x16_bf16 v[16:31], v[34:37], v[116:119], v[16:31]
	v_or_b32_e32 v34, 0x60, v150
	v_bitop3_b32 v34, v34, v32, v42 bitop3:0xde
	v_add_u32_e32 v165, 0, v34
	s_waitcnt lgkmcnt(0)
	v_mfma_f32_32x32x16_bf16 v[0:15], v[38:41], v[116:119], v[0:15]
	ds_read_b128 v[34:37], v165 offset:32768
	ds_read_b128 v[38:41], v165 offset:40960
	s_waitcnt lgkmcnt(1)
	v_mfma_f32_32x32x16_bf16 v[16:31], v[34:37], v[112:115], v[16:31]
	v_or_b32_e32 v34, 0x80, v150
	v_bitop3_b32 v34, v34, v32, v42 bitop3:0xde
	v_add_u32_e32 v164, 0, v34
	s_waitcnt lgkmcnt(0)
	v_mfma_f32_32x32x16_bf16 v[0:15], v[38:41], v[112:115], v[0:15]
	ds_read_b128 v[34:37], v164 offset:32768
	ds_read_b128 v[38:41], v164 offset:40960
	s_waitcnt lgkmcnt(1)
	v_mfma_f32_32x32x16_bf16 v[16:31], v[34:37], v[108:111], v[16:31]
	v_or_b32_e32 v34, 0xa0, v150
	v_bitop3_b32 v34, v34, v32, v42 bitop3:0xde
	v_add_u32_e32 v163, 0, v34
	s_waitcnt lgkmcnt(0)
	v_mfma_f32_32x32x16_bf16 v[0:15], v[38:41], v[108:111], v[0:15]
	ds_read_b128 v[34:37], v163 offset:32768
	ds_read_b128 v[38:41], v163 offset:40960
	s_waitcnt lgkmcnt(1)
	v_mfma_f32_32x32x16_bf16 v[16:31], v[34:37], v[104:107], v[16:31]
	v_or_b32_e32 v34, 0xc0, v150
	v_bitop3_b32 v34, v34, v32, v42 bitop3:0xde
	v_add_u32_e32 v162, 0, v34
	s_waitcnt lgkmcnt(0)
	v_mfma_f32_32x32x16_bf16 v[0:15], v[38:41], v[104:107], v[0:15]
	ds_read_b128 v[34:37], v162 offset:32768
	ds_read_b128 v[38:41], v162 offset:40960
	s_waitcnt lgkmcnt(1)
	v_mfma_f32_32x32x16_bf16 v[16:31], v[34:37], v[100:103], v[16:31]
	v_or_b32_e32 v34, 0xe0, v150
	v_bitop3_b32 v32, v34, v32, v42 bitop3:0xde
	v_add_u32_e32 v161, 0, v32
	v_add_u32_e32 v32, s4, v148
	s_waitcnt lgkmcnt(0)
	v_mfma_f32_32x32x16_bf16 v[0:15], v[38:41], v[100:103], v[0:15]
	ds_read_b128 v[34:37], v161 offset:32768
	ds_read_b128 v[38:41], v161 offset:40960
	s_waitcnt lgkmcnt(1)
	v_mfma_f32_32x32x16_bf16 v[16:31], v[34:37], v[96:99], v[16:31]
	s_waitcnt lgkmcnt(0)
	v_mfma_f32_32x32x16_bf16 v[0:15], v[38:41], v[96:99], v[0:15]
	s_cbranch_scc1 .LBB0_638
	s_sub_i32 s0, s5, 31
	v_add_u32_e32 v34, 0x41, v32
	v_cmp_lt_i32_e32 vcc, s0, v32
	v_cmp_gt_i32_e64 s[0:1], s19, v34
	s_or_b64 s[8:9], vcc, s[0:1]
	s_and_saveexec_b64 s[0:1], s[8:9]
	s_cbranch_execz .LBB0_637
	v_lshlrev_b32_e32 v34, 2, v155
	v_or_b32_e32 v35, v32, v154
	v_sub_u32_e32 v34, v34, v35
	v_add_u32_e32 v35, s19, v34
	v_add_u32_e32 v34, s5, v34
	s_movk_i32 s3, 0x101
	v_cmp_gt_u32_e32 vcc, s3, v34
	v_add_u32_e32 v34, 0xa0, v35
	s_nop 0
	v_cndmask_b32_e32 v16, v217, v16, vcc
	v_cmp_gt_u32_e32 vcc, s3, v34
	v_add_u32_e32 v34, 0x81, v35
	s_nop 0
	v_cndmask_b32_e32 v0, v217, v0, vcc
	v_cmp_gt_u32_e32 vcc, s3, v34
	v_add_u32_e32 v34, 0xa1, v35
	s_nop 0
	v_cndmask_b32_e32 v17, v217, v17, vcc
	v_cmp_gt_u32_e32 vcc, s3, v34
	v_add_u32_e32 v34, 0x82, v35
	s_nop 0
	v_cndmask_b32_e32 v1, v217, v1, vcc
	v_cmp_gt_u32_e32 vcc, s3, v34
	v_add_u32_e32 v34, 0xa2, v35
	s_nop 0
	v_cndmask_b32_e32 v18, v217, v18, vcc
	v_cmp_gt_u32_e32 vcc, s3, v34
	v_add_u32_e32 v34, 0x83, v35
	s_nop 0
	v_cndmask_b32_e32 v2, v217, v2, vcc
	v_cmp_gt_u32_e32 vcc, s3, v34
	v_add_u32_e32 v34, 0xa3, v35
	s_nop 0
	v_cndmask_b32_e32 v19, v217, v19, vcc
	v_cmp_gt_u32_e32 vcc, s3, v34
	v_add_u32_e32 v34, 0x88, v35
	s_nop 0
	v_cndmask_b32_e32 v3, v217, v3, vcc
	v_cmp_gt_u32_e32 vcc, s3, v34
	v_add_u32_e32 v34, 0xa8, v35
	s_nop 0
	v_cndmask_b32_e32 v20, v217, v20, vcc
	v_cmp_gt_u32_e32 vcc, s3, v34
	v_add_u32_e32 v34, 0x89, v35
	s_nop 0
	v_cndmask_b32_e32 v4, v217, v4, vcc
	v_cmp_gt_u32_e32 vcc, s3, v34
	v_add_u32_e32 v34, 0xa9, v35
	s_nop 0
	v_cndmask_b32_e32 v21, v217, v21, vcc
	v_cmp_gt_u32_e32 vcc, s3, v34
	v_add_u32_e32 v34, 0x8a, v35
	s_nop 0
	v_cndmask_b32_e32 v5, v217, v5, vcc
	v_cmp_gt_u32_e32 vcc, s3, v34
	v_add_u32_e32 v34, 0xaa, v35
	s_nop 0
	v_cndmask_b32_e32 v22, v217, v22, vcc
	v_cmp_gt_u32_e32 vcc, s3, v34
	v_add_u32_e32 v34, 0x8b, v35
	s_nop 0
	v_cndmask_b32_e32 v6, v217, v6, vcc
	v_cmp_gt_u32_e32 vcc, s3, v34
	v_add_u32_e32 v34, 0xab, v35
	s_nop 0
	v_cndmask_b32_e32 v23, v217, v23, vcc
	v_cmp_gt_u32_e32 vcc, s3, v34
	v_add_u32_e32 v34, 0x90, v35
	s_nop 0
	v_cndmask_b32_e32 v7, v217, v7, vcc
	v_cmp_gt_u32_e32 vcc, s3, v34
	v_add_u32_e32 v34, 0xb0, v35
	s_nop 0
	v_cndmask_b32_e32 v24, v217, v24, vcc
	v_cmp_gt_u32_e32 vcc, s3, v34
	v_add_u32_e32 v34, 0x91, v35
	s_nop 0
	v_cndmask_b32_e32 v8, v217, v8, vcc
	v_cmp_gt_u32_e32 vcc, s3, v34
	v_add_u32_e32 v34, 0xb1, v35
	s_nop 0
	v_cndmask_b32_e32 v25, v217, v25, vcc
	v_cmp_gt_u32_e32 vcc, s3, v34
	v_add_u32_e32 v34, 0x92, v35
	s_nop 0
	v_cndmask_b32_e32 v9, v217, v9, vcc
	v_cmp_gt_u32_e32 vcc, s3, v34
	v_add_u32_e32 v34, 0xb2, v35
	s_nop 0
	v_cndmask_b32_e32 v26, v217, v26, vcc
	v_cmp_gt_u32_e32 vcc, s3, v34
	v_add_u32_e32 v34, 0x93, v35
	s_nop 0
	v_cndmask_b32_e32 v10, v217, v10, vcc
	v_cmp_gt_u32_e32 vcc, s3, v34
	v_add_u32_e32 v34, 0xb3, v35
	s_nop 0
	v_cndmask_b32_e32 v27, v217, v27, vcc
	v_cmp_gt_u32_e32 vcc, s3, v34
	v_add_u32_e32 v34, 0x98, v35
	s_nop 0
	v_cndmask_b32_e32 v11, v217, v11, vcc
	v_cmp_gt_u32_e32 vcc, s3, v34
	v_add_u32_e32 v34, 0xb8, v35
	s_nop 0
	v_cndmask_b32_e32 v28, v217, v28, vcc
	v_cmp_gt_u32_e32 vcc, s3, v34
	v_add_u32_e32 v34, 0x99, v35
	s_nop 0
	v_cndmask_b32_e32 v12, v217, v12, vcc
	v_cmp_gt_u32_e32 vcc, s3, v34
	v_add_u32_e32 v34, 0xb9, v35
	s_nop 0
	v_cndmask_b32_e32 v29, v217, v29, vcc
	v_cmp_gt_u32_e32 vcc, s3, v34
	v_add_u32_e32 v34, 0x9a, v35
	s_nop 0
	v_cndmask_b32_e32 v13, v217, v13, vcc
	v_cmp_gt_u32_e32 vcc, s3, v34
	v_add_u32_e32 v34, 0xba, v35
	s_nop 0
	v_cndmask_b32_e32 v30, v217, v30, vcc
	v_cmp_gt_u32_e32 vcc, s3, v34
	v_add_u32_e32 v34, 0x9b, v35
	s_nop 0
	v_cndmask_b32_e32 v14, v217, v14, vcc
	v_cmp_gt_u32_e32 vcc, s3, v34
	v_add_u32_e32 v34, 0xbb, v35
	s_nop 0
	v_cndmask_b32_e32 v31, v217, v31, vcc
	v_cmp_gt_u32_e32 vcc, s3, v34
	s_nop 1
	v_cndmask_b32_e32 v15, v217, v15, vcc

.LBB0_676:
	s_ashr_i32 s5, s4, 31
	s_lshl_b64 s[4:5], s[4:5], 1
	s_add_u32 s4, s10, s4
	s_addc_u32 s5, s11, s5
	s_ashr_i32 s3, s2, 31
	s_lshl_b64 s[2:3], s[2:3], 1
	s_add_u32 s7, s34, s2
	s_addc_u32 s20, s35, s3
	s_ashr_i32 s1, s0, 31
	s_lshl_b64 s[0:1], s[0:1], 1
	s_add_u32 s21, s34, s0
	s_mov_b32 s26, s22
	s_addc_u32 s22, s35, s1
	v_and_b32_e32 v1, 0x3fffffc0, v0
	s_add_i32 s0, 0, 0x10000
	v_ashrrev_i32_e32 v144, 1, v0
	v_bfe_u32 v155, v0, 5, 1
	v_lshl_add_u32 v156, v1, 2, s0
	v_bfi_b32 v1, s67, v144, v0
	v_mov_b64_e32 v[2:3], s[4:5]
	v_mad_i64_i32 v[2:3], s[0:1], v1, s66, v[2:3]
	v_lshlrev_b32_e32 v148, 4, v155
	v_mov_b32_e32 v149, v193
	v_ashrrev_i32_e32 v1, 4, v0
	v_lshl_add_u64 v[2:3], v[2:3], 0, v[148:149]
	v_and_b32_e32 v4, 0xfffff0, v1
	v_lshlrev_b32_e32 v5, 1, v1
	global_load_dwordx4 v[124:127], v[2:3], off
	global_load_dwordx4 v[120:123], v[2:3], off offset:32
	global_load_dwordx4 v[116:119], v[2:3], off offset:64
	global_load_dwordx4 v[112:115], v[2:3], off offset:96
	global_load_dwordx4 v[108:111], v[2:3], off offset:128
	global_load_dwordx4 v[104:107], v[2:3], off offset:160
	global_load_dwordx4 v[100:103], v[2:3], off offset:192
	global_load_dwordx4 v[96:99], v[2:3], off offset:224
	v_lshlrev_b32_e32 v2, 3, v0
	v_and_or_b32 v4, v5, 8, v4
	v_and_b32_e32 v3, 0x78, v2
	v_lshrrev_b32_e32 v5, 1, v1
	v_lshrrev_b32_e32 v4, 1, v4
	v_bfe_u32 v2, v2, 5, 2
	v_and_b32_e32 v6, 3, v1
	v_or_b32_e32 v4, v4, v2
	v_and_or_b32 v5, v5, 4, v6
	v_lshlrev_b32_e32 v18, 1, v3
	v_lshlrev_b32_e32 v4, 9, v4
	v_lshlrev_b32_e32 v5, 6, v5
	v_and_b32_e32 v6, 48, v18
	v_add_u32_e32 v20, 32, v1
	v_or3_b32 v19, v4, v5, v6
	v_and_b32_e32 v4, 0xfffff0, v20
	v_lshlrev_b32_e32 v7, 1, v20
	v_and_or_b32 v4, v7, 8, v4
	v_lshrrev_b32_e32 v4, 1, v4
	v_or_b32_e32 v2, v4, v2
	v_and_b32_e32 v32, 63, v0
	v_lshlrev_b32_e32 v2, 9, v2
	v_lshlrev_b32_e32 v22, 4, v0
	v_or3_b32 v21, v2, v5, v6
	v_lshlrev_b32_e32 v2, 3, v32
	v_and_b32_e32 v4, 0xc0, v22
	v_lshlrev_b32_e32 v5, 1, v0
	v_and_or_b32 v4, v2, 24, v4
	v_and_b32_e32 v5, 32, v5
	v_and_b32_e32 v2, 0x100, v2
	s_cmp_lg_u32 0, -1
	v_or3_b32 v145, v4, v5, v2
	s_cselect_b32 s0, 0, 0
	v_add_u32_e32 v149, s0, v145
	s_add_u32 s0, s7, 0x9000000
	v_mul_lo_u32 v2, v1, s68
	s_addc_u32 s1, s20, 0
	v_or_b32_e32 v2, v2, v3
	s_add_u32 s2, s21, 0x9000000
	v_lshlrev_b32_e32 v192, 1, v2
	s_addc_u32 s3, s22, 0
	v_add_u32_e32 v150, 0x48000, v192
	global_load_dwordx4 v[2:5], v192, s[2:3]
	global_load_dwordx4 v[6:9], v150, s[2:3]
	global_load_dwordx4 v[10:13], v192, s[0:1]
	global_load_dwordx4 v[14:17], v150, s[0:1]
	v_and_b32_e32 v154, 31, v0
	v_lshlrev_b32_e32 v1, 8, v1
	v_and_b32_e32 v0, 0xf0, v0
	v_bitop3_b32 v1, v18, v1, v0 bitop3:0xde
	v_add_u32_e32 v170, 0, v1
	v_lshlrev_b32_e32 v1, 8, v20
	v_bitop3_b32 v0, v18, v1, v0 bitop3:0xde
	v_lshlrev_b32_e32 v33, 8, v154
	v_and_b32_e32 v42, 0xf0, v22
	v_add_u32_e32 v171, 0, v0
	v_bitop3_b32 v0, v148, v33, v42 bitop3:0xde
	v_add_u32_e32 v161, 0, v19
	v_add_u32_e32 v162, 0, v21
	v_add_u32_e32 v160, 0, v0
	s_waitcnt vmcnt(0)
	v_or_b32_e32 v34, 32, v148
	v_bitop3_b32 v34, v34, v33, v42 bitop3:0xde
	v_add_u32_e32 v163, 0, v34
	s_mov_b32 s23, 0x42b504f3
	v_lshl_add_u32 v157, v154, 2, v156
	s_waitcnt vmcnt(3)
	ds_write_b128 v161, v[2:5]
	s_waitcnt vmcnt(2)
	ds_write_b128 v162, v[6:9]
	s_waitcnt vmcnt(1)
	ds_write_b128 v170, v[10:13] offset:32768
	s_waitcnt vmcnt(0)
	ds_write_b128 v171, v[14:17] offset:32768
	s_waitcnt lgkmcnt(0)
	s_barrier
	ds_read_b128 v[0:3], v160 offset:32768
	ds_read_b128 v[4:7], v160 offset:40960
	s_waitcnt lgkmcnt(1)
	v_mfma_f32_32x32x16_bf16 v[16:31], v[0:3], v[124:127], 0
	ds_read_b128 v[34:37], v163 offset:32768
	ds_read_b128 v[38:41], v163 offset:40960
	s_waitcnt lgkmcnt(2)
	v_mfma_f32_32x32x16_bf16 v[0:15], v[4:7], v[124:127], 0
	s_waitcnt lgkmcnt(1)
	v_mfma_f32_32x32x16_bf16 v[16:31], v[34:37], v[120:123], v[16:31]
	v_or_b32_e32 v34, 64, v148
	v_bitop3_b32 v34, v34, v33, v42 bitop3:0xde
	v_add_u32_e32 v164, 0, v34
	s_waitcnt lgkmcnt(0)
	v_mfma_f32_32x32x16_bf16 v[0:15], v[38:41], v[120:123], v[0:15]
	ds_read_b128 v[34:37], v164 offset:32768
	ds_read_b128 v[38:41], v164 offset:40960
	s_waitcnt lgkmcnt(1)
	v_mfma_f32_32x32x16_bf16 v[16:31], v[34:37], v[116:119], v[16:31]
	v_or_b32_e32 v34, 0x60, v148
	v_bitop3_b32 v34, v34, v33, v42 bitop3:0xde
	v_add_u32_e32 v165, 0, v34
	s_waitcnt lgkmcnt(0)
	v_mfma_f32_32x32x16_bf16 v[0:15], v[38:41], v[116:119], v[0:15]
	ds_read_b128 v[34:37], v165 offset:32768
	ds_read_b128 v[38:41], v165 offset:40960
	s_waitcnt lgkmcnt(1)
	v_mfma_f32_32x32x16_bf16 v[16:31], v[34:37], v[112:115], v[16:31]
	v_or_b32_e32 v34, 0x80, v148
	v_bitop3_b32 v34, v34, v33, v42 bitop3:0xde
	v_add_u32_e32 v166, 0, v34
	s_waitcnt lgkmcnt(0)
	v_mfma_f32_32x32x16_bf16 v[0:15], v[38:41], v[112:115], v[0:15]
	ds_read_b128 v[34:37], v166 offset:32768
	ds_read_b128 v[38:41], v166 offset:40960
	s_waitcnt lgkmcnt(1)
	v_mfma_f32_32x32x16_bf16 v[16:31], v[34:37], v[108:111], v[16:31]
	v_or_b32_e32 v34, 0xa0, v148
	v_bitop3_b32 v34, v34, v33, v42 bitop3:0xde
	v_add_u32_e32 v167, 0, v34
	s_waitcnt lgkmcnt(0)
	v_mfma_f32_32x32x16_bf16 v[0:15], v[38:41], v[108:111], v[0:15]
	ds_read_b128 v[34:37], v167 offset:32768
	ds_read_b128 v[38:41], v167 offset:40960
	s_waitcnt lgkmcnt(1)
	v_mfma_f32_32x32x16_bf16 v[16:31], v[34:37], v[104:107], v[16:31]
	v_or_b32_e32 v34, 0xc0, v148
	v_bitop3_b32 v34, v34, v33, v42 bitop3:0xde
	v_add_u32_e32 v168, 0, v34
	s_waitcnt lgkmcnt(0)
	v_mfma_f32_32x32x16_bf16 v[0:15], v[38:41], v[104:107], v[0:15]
	ds_read_b128 v[34:37], v168 offset:32768
	ds_read_b128 v[38:41], v168 offset:40960
	s_waitcnt lgkmcnt(1)
	v_mfma_f32_32x32x16_bf16 v[16:31], v[34:37], v[100:103], v[16:31]
	v_or_b32_e32 v34, 0xe0, v148
	v_bitop3_b32 v33, v34, v33, v42 bitop3:0xde
	v_add_u32_e32 v169, 0, v33
	s_waitcnt lgkmcnt(0)
	v_mfma_f32_32x32x16_bf16 v[0:15], v[38:41], v[100:103], v[0:15]
	ds_read_b128 v[34:37], v169 offset:32768
	ds_read_b128 v[38:41], v169 offset:40960
	s_waitcnt lgkmcnt(1)
	v_mfma_f32_32x32x16_bf16 v[16:31], v[34:37], v[96:99], v[16:31]
	s_waitcnt lgkmcnt(0)
	v_mfma_f32_32x32x16_bf16 v[0:15], v[38:41], v[96:99], v[0:15]
	s_nop 9
	v_max_f32_e32 v33, v17, v17
	v_max_f32_e32 v34, v16, v16
	v_max_f32_e32 v33, v34, v33
	v_max3_f32 v33, v33, v18, v19
	v_max3_f32 v33, v33, v20, v21
	v_max3_f32 v33, v33, v22, v23
	v_max3_f32 v33, v33, v24, v25
	v_max3_f32 v33, v33, v26, v27
	v_max3_f32 v33, v33, v28, v29
	v_max3_f32 v33, v33, v30, v31
	v_max3_f32 v33, v33, v0, v1
	v_max3_f32 v33, v33, v2, v3
	v_max3_f32 v33, v33, v4, v5
	v_max3_f32 v33, v33, v6, v7
	v_max3_f32 v33, v33, v8, v9
	v_max3_f32 v33, v33, v10, v11
	v_max3_f32 v33, v33, v12, v13
	v_max3_f32 v33, v33, v14, v15
	v_mov_b32_e32 v34, v33
	s_nop 1
	v_permlane32_swap_b32_e32 v33, v34
	v_max_f32_e32 v34, v34, v34
	v_max_f32_e32 v33, v33, v33
	v_max_f32_e32 v33, v33, v34
	v_add_f32_e32 v34, 0x7149f2ca, v33
	v_cmp_ge_f32_e32 vcc, s23, v34
	s_cmp_eq_u64 vcc, exec
	s_cselect_b64 s[0:1], -1, 0
	v_max_f32_e32 v147, 0xf149f2ca, v33
	v_mov_b32_e32 v33, 0xf149f2ca
	s_add_u32 s2, s7, 0x9090000
	v_cndmask_b32_e64 v146, v147, v33, s[0:1]
	s_addc_u32 s3, s20, 0
	v_mul_f32_e32 v33, 0xbe0293ee, v146
	s_add_u32 s4, s21, 0x9090000
	v_fmamk_f32 v34, v16, 0x3e0293ee, v33
	v_fmamk_f32 v35, v17, 0x3e0293ee, v33
	v_fmamk_f32 v36, v18, 0x3e0293ee, v33
	v_fmamk_f32 v37, v19, 0x3e0293ee, v33
	v_fmamk_f32 v38, v20, 0x3e0293ee, v33
	v_fmamk_f32 v39, v21, 0x3e0293ee, v33
	v_fmamk_f32 v40, v22, 0x3e0293ee, v33
	v_fmamk_f32 v41, v23, 0x3e0293ee, v33
	v_fmamk_f32 v42, v24, 0x3e0293ee, v33
	v_fmamk_f32 v43, v25, 0x3e0293ee, v33
	v_fmamk_f32 v44, v26, 0x3e0293ee, v33
	v_fmamk_f32 v45, v27, 0x3e0293ee, v33
	v_fmamk_f32 v46, v28, 0x3e0293ee, v33
	v_fmamk_f32 v47, v29, 0x3e0293ee, v33
	v_fmamk_f32 v48, v30, 0x3e0293ee, v33
	s_addc_u32 s5, s22, 0
	v_fmamk_f32 v31, v31, 0x3e0293ee, v33
	v_fmamk_f32 v26, v0, 0x3e0293ee, v33
	v_fmamk_f32 v27, v1, 0x3e0293ee, v33
	v_fmamk_f32 v28, v2, 0x3e0293ee, v33
	v_fmamk_f32 v29, v3, 0x3e0293ee, v33
	v_fmamk_f32 v30, v4, 0x3e0293ee, v33
	v_fmamk_f32 v19, v5, 0x3e0293ee, v33
	v_fmamk_f32 v20, v6, 0x3e0293ee, v33
	v_fmamk_f32 v21, v7, 0x3e0293ee, v33
	v_fmamk_f32 v22, v8, 0x3e0293ee, v33
	v_fmamk_f32 v23, v9, 0x3e0293ee, v33
	v_fmamk_f32 v24, v10, 0x3e0293ee, v33
	v_fmamk_f32 v25, v11, 0x3e0293ee, v33
	v_fmamk_f32 v16, v12, 0x3e0293ee, v33
	v_fmamk_f32 v17, v13, 0x3e0293ee, v33
	v_fmamk_f32 v18, v14, 0x3e0293ee, v33
	v_fmac_f32_e32 v33, 0x3e0293ee, v15
	v_exp_f32_e32 v9, v34
	v_exp_f32_e32 v11, v35
	v_exp_f32_e32 v12, v36
	v_exp_f32_e32 v13, v37
	v_exp_f32_e32 v14, v38
	v_exp_f32_e32 v15, v39
	v_exp_f32_e32 v8, v40
	v_exp_f32_e32 v10, v41
	v_exp_f32_e32 v3, v42
	v_exp_f32_e32 v5, v43
	v_exp_f32_e32 v6, v44
	v_exp_f32_e32 v7, v45
	v_exp_f32_e32 v0, v46
	v_exp_f32_e32 v1, v47
	v_exp_f32_e32 v2, v48
	global_load_dwordx4 v[34:37], v192, s[4:5]
	global_load_dwordx4 v[38:41], v150, s[4:5]
	global_load_dwordx4 v[42:45], v192, s[2:3]
	global_load_dwordx4 v[46:49], v150, s[2:3]
	v_exp_f32_e32 v4, v31
	s_waitcnt vmcnt(0)
	v_cmp_gt_u32_e64 s[2:3], 32, v32
	s_waitcnt vmcnt(3)
	ds_write_b128 v161, v[34:37] offset:16384
	s_waitcnt vmcnt(2)
	ds_write_b128 v162, v[38:41] offset:16384
	s_waitcnt vmcnt(1)
	ds_write_b128 v170, v[42:45] offset:49152
	s_waitcnt vmcnt(0)
	ds_write_b128 v171, v[46:49] offset:49152
	s_waitcnt lgkmcnt(0)
	s_barrier
	ds_read_b128 v[34:37], v160 offset:49152
	ds_read_b128 v[38:41], v160 offset:57344
	v_add_f32_e32 v32, 0, v9
	v_add_f32_e32 v32, v11, v32
	v_add_f32_e32 v32, v12, v32
	s_waitcnt lgkmcnt(1)
	v_mfma_f32_32x32x16_bf16 v[80:95], v[34:37], v[124:127], 0
	v_add_f32_e32 v32, v13, v32
	v_add_f32_e32 v32, v14, v32
	v_add_f32_e32 v32, v15, v32
	v_add_f32_e32 v32, v8, v32
	v_add_f32_e32 v32, v10, v32
	v_add_f32_e32 v32, v3, v32
	v_add_f32_e32 v32, v5, v32
	s_waitcnt lgkmcnt(0)
	v_mfma_f32_32x32x16_bf16 v[64:79], v[38:41], v[124:127], 0
	ds_read_b128 v[34:37], v163 offset:49152
	ds_read_b128 v[38:41], v163 offset:57344
	v_add_f32_e32 v32, v6, v32
	v_add_f32_e32 v32, v7, v32
	v_exp_f32_e32 v26, v26
	v_add_f32_e32 v32, v0, v32
	v_exp_f32_e32 v27, v27
	v_add_f32_e32 v32, v1, v32
	s_waitcnt lgkmcnt(1)
	v_mfma_f32_32x32x16_bf16 v[80:95], v[34:37], v[120:123], v[80:95]
	v_exp_f32_e32 v28, v28
	v_add_f32_e32 v32, v2, v32
	v_exp_f32_e32 v29, v29
	v_add_f32_e32 v32, v4, v32
	v_exp_f32_e32 v30, v30
	v_add_f32_e32 v32, v26, v32
	v_exp_f32_e32 v19, v19
	s_waitcnt lgkmcnt(0)
	v_mfma_f32_32x32x16_bf16 v[64:79], v[38:41], v[120:123], v[64:79]
	ds_read_b128 v[34:37], v164 offset:49152
	ds_read_b128 v[38:41], v164 offset:57344
	v_add_f32_e32 v32, v27, v32
	v_exp_f32_e32 v20, v20
	v_add_f32_e32 v32, v28, v32
	v_exp_f32_e32 v21, v21
	v_add_f32_e32 v32, v29, v32
	v_exp_f32_e32 v22, v22
	s_waitcnt lgkmcnt(1)
	v_mfma_f32_32x32x16_bf16 v[80:95], v[34:37], v[116:119], v[80:95]
	v_add_f32_e32 v32, v30, v32
	v_exp_f32_e32 v23, v23
	v_add_f32_e32 v32, v19, v32
	v_exp_f32_e32 v24, v24
	v_add_f32_e32 v32, v20, v32
	v_exp_f32_e32 v25, v25
	v_add_f32_e32 v32, v21, v32
	s_waitcnt lgkmcnt(0)
	v_mfma_f32_32x32x16_bf16 v[64:79], v[38:41], v[116:119], v[64:79]
	ds_read_b128 v[34:37], v165 offset:49152
	ds_read_b128 v[38:41], v165 offset:57344
	v_exp_f32_e32 v16, v16
	v_add_f32_e32 v32, v22, v32
	v_exp_f32_e32 v17, v17
	v_add_f32_e32 v32, v23, v32
	v_exp_f32_e32 v18, v18
	v_add_f32_e32 v32, v24, v32
	s_waitcnt lgkmcnt(1)
	v_mfma_f32_32x32x16_bf16 v[80:95], v[34:37], v[112:115], v[80:95]
	v_exp_f32_e32 v31, v33
	v_add_f32_e32 v32, v25, v32
	v_add_f32_e32 v32, v16, v32
	v_add_f32_e32 v32, v17, v32
	v_add_f32_e32 v32, v18, v32
	v_add_f32_e32 v158, v31, v32
	v_mov_b32_e32 v159, v158
	s_waitcnt lgkmcnt(0)
	v_mfma_f32_32x32x16_bf16 v[64:79], v[38:41], v[112:115], v[64:79]
	ds_read_b128 v[34:37], v166 offset:49152
	ds_read_b128 v[38:41], v166 offset:57344
	v_permlane32_swap_b32_e32 v158, v159
	s_waitcnt lgkmcnt(1)
	v_mfma_f32_32x32x16_bf16 v[80:95], v[34:37], v[108:111], v[80:95]
	s_waitcnt lgkmcnt(0)
	v_mfma_f32_32x32x16_bf16 v[64:79], v[38:41], v[108:111], v[64:79]
	ds_read_b128 v[34:37], v167 offset:49152
	ds_read_b128 v[38:41], v167 offset:57344
	s_waitcnt lgkmcnt(1)
	v_mfma_f32_32x32x16_bf16 v[80:95], v[34:37], v[104:107], v[80:95]
	s_waitcnt lgkmcnt(0)
	v_mfma_f32_32x32x16_bf16 v[64:79], v[38:41], v[104:107], v[64:79]
	ds_read_b128 v[34:37], v168 offset:49152
	ds_read_b128 v[38:41], v168 offset:57344
	s_waitcnt lgkmcnt(1)
	v_mfma_f32_32x32x16_bf16 v[80:95], v[34:37], v[100:103], v[80:95]
	s_waitcnt lgkmcnt(0)
	v_mfma_f32_32x32x16_bf16 v[64:79], v[38:41], v[100:103], v[64:79]
	ds_read_b128 v[34:37], v169 offset:49152
	ds_read_b128 v[38:41], v169 offset:57344
	v_cvt_pk_bf16_f32 v48, v9, v11
	v_cvt_pk_bf16_f32 v49, v12, v13
	v_cvt_pk_bf16_f32 v50, v14, v15
	v_cvt_pk_bf16_f32 v51, v8, v10
	v_cvt_pk_bf16_f32 v172, v3, v5
	v_cvt_pk_bf16_f32 v173, v6, v7
	s_waitcnt lgkmcnt(1)
	v_mfma_f32_32x32x16_bf16 v[80:95], v[34:37], v[96:99], v[80:95]
	v_cvt_pk_bf16_f32 v174, v0, v1
	v_permlane32_swap_b32_e32 v48, v50
	v_permlane32_swap_b32_e32 v49, v51
	v_cvt_pk_bf16_f32 v175, v2, v4
	v_permlane32_swap_b32_e32 v172, v174
	s_waitcnt lgkmcnt(0)
	v_mfma_f32_32x32x16_bf16 v[64:79], v[38:41], v[96:99], v[64:79]
	v_cvt_pk_bf16_f32 v176, v26, v27
	v_cvt_pk_bf16_f32 v177, v28, v29
	v_cvt_pk_bf16_f32 v178, v30, v19
	v_cvt_pk_bf16_f32 v179, v20, v21
	v_cvt_pk_bf16_f32 v180, v22, v23
	v_cvt_pk_bf16_f32 v181, v24, v25
	v_cvt_pk_bf16_f32 v182, v16, v17
	v_cvt_pk_bf16_f32 v183, v18, v31
	v_permlane32_swap_b32_e32 v173, v175
	v_permlane32_swap_b32_e32 v176, v178
	v_permlane32_swap_b32_e32 v177, v179
	v_permlane32_swap_b32_e32 v180, v182
	v_permlane32_swap_b32_e32 v181, v183
	s_add_u32 s4, s7, 0x9120000
	s_addc_u32 s5, s20, 0
	s_add_u32 s8, s21, 0x9120000
	s_addc_u32 s9, s22, 0
	global_load_dwordx4 v[128:131], v192, s[8:9]
	global_load_dwordx4 v[132:135], v192, s[4:5]
	global_load_dwordx4 v[140:143], v150, s[8:9]
	global_load_dwordx4 v[136:139], v150, s[4:5]
	ds_read_b64_tr_b16 v[0:1], v149 offset:0
	ds_read_b64_tr_b16 v[2:3], v149 offset:0x800
	ds_read_b64_tr_b16 v[16:17], v149 offset:0x1000
	ds_read_b64_tr_b16 v[18:19], v149 offset:0x1800
	ds_read_b64_tr_b16 v[20:21], v149 offset:0x2000
	ds_read_b64_tr_b16 v[22:23], v149 offset:0x2800
	ds_read_b64_tr_b16 v[24:25], v149 offset:0x3000
	ds_read_b64_tr_b16 v[26:27], v149 offset:0x3800
	s_waitcnt lgkmcnt(0)
	s_nop 0
	v_mfma_f32_32x32x16_bf16 v[0:15], v[48:51], v[0:3], 0
	v_mfma_f32_32x32x16_bf16 v[0:15], v[172:175], v[16:19], v[0:15]
	ds_read_b64_tr_b16 v[16:17], v149 offset:0x200
	ds_read_b64_tr_b16 v[18:19], v149 offset:0xa00
	ds_read_b64_tr_b16 v[32:33], v149 offset:0x1200
	ds_read_b64_tr_b16 v[34:35], v149 offset:0x1a00
	ds_read_b64_tr_b16 v[36:37], v149 offset:0x2200
	ds_read_b64_tr_b16 v[38:39], v149 offset:0x2a00
	ds_read_b64_tr_b16 v[40:41], v149 offset:0x3200
	v_mfma_f32_32x32x16_bf16 v[0:15], v[176:179], v[20:23], v[0:15]
	ds_read_b64_tr_b16 v[42:43], v149 offset:0x3a00
	s_waitcnt lgkmcnt(0)
	v_mfma_f32_32x32x16_bf16 v[0:15], v[180:183], v[24:27], v[0:15]
	v_mfma_f32_32x32x16_bf16 v[16:31], v[48:51], v[16:19], 0
	v_mfma_f32_32x32x16_bf16 v[16:31], v[172:175], v[32:35], v[16:31]
	ds_read_b64_tr_b16 v[32:33], v149 offset:0x400
	ds_read_b64_tr_b16 v[34:35], v149 offset:0xc00
	ds_read_b64_tr_b16 v[52:53], v149 offset:0x1400
	ds_read_b64_tr_b16 v[54:55], v149 offset:0x1c00
	ds_read_b64_tr_b16 v[56:57], v149 offset:0x2400
	ds_read_b64_tr_b16 v[58:59], v149 offset:0x2c00
	ds_read_b64_tr_b16 v[60:61], v149 offset:0x3400
	v_mfma_f32_32x32x16_bf16 v[16:31], v[176:179], v[36:39], v[16:31]
	ds_read_b64_tr_b16 v[62:63], v149 offset:0x3c00
	s_waitcnt lgkmcnt(0)
	v_mfma_f32_32x32x16_bf16 v[16:31], v[180:183], v[40:43], v[16:31]
	v_mfma_f32_32x32x16_bf16 v[32:47], v[48:51], v[32:35], 0
	v_mfma_f32_32x32x16_bf16 v[32:47], v[172:175], v[52:55], v[32:47]
	ds_read_b64_tr_b16 v[52:53], v149 offset:0x600
	ds_read_b64_tr_b16 v[54:55], v149 offset:0xe00
	ds_read_b64_tr_b16 v[184:185], v149 offset:0x1600
	ds_read_b64_tr_b16 v[186:187], v149 offset:0x1e00
	ds_read_b64_tr_b16 v[188:189], v149 offset:0x2600
	ds_read_b64_tr_b16 v[190:191], v149 offset:0x2e00
	ds_read_b64_tr_b16 v[200:201], v149 offset:0x3600
	v_mfma_f32_32x32x16_bf16 v[32:47], v[176:179], v[56:59], v[32:47]
	ds_read_b64_tr_b16 v[202:203], v149 offset:0x3e00
	s_waitcnt lgkmcnt(0)
	v_mfma_f32_32x32x16_bf16 v[32:47], v[180:183], v[60:63], v[32:47]
	v_mfma_f32_32x32x16_bf16 v[48:63], v[48:51], v[52:55], 0
	v_max_f32_e32 v151, v81, v81
	v_max_f32_e32 v152, v80, v80
	v_max_f32_e32 v151, v152, v151
	v_max3_f32 v151, v151, v82, v83
	v_max3_f32 v151, v151, v84, v85
	v_max3_f32 v151, v151, v86, v87
	v_max3_f32 v151, v151, v88, v89
	v_mfma_f32_32x32x16_bf16 v[48:63], v[172:175], v[184:187], v[48:63]
	v_max3_f32 v151, v151, v90, v91
	v_max3_f32 v151, v151, v92, v93
	v_max3_f32 v151, v151, v94, v95
	v_max3_f32 v151, v151, v64, v65
	v_max3_f32 v151, v151, v66, v67
	v_max3_f32 v151, v151, v68, v69
	v_max3_f32 v151, v151, v70, v71
	v_max3_f32 v151, v151, v72, v73
	v_mfma_f32_32x32x16_bf16 v[48:63], v[176:179], v[188:191], v[48:63]
	v_max3_f32 v151, v151, v74, v75
	v_max3_f32 v151, v151, v76, v77
	v_max3_f32 v151, v151, v78, v79
	v_mov_b32_e32 v152, v151
	s_nop 1
	v_permlane32_swap_b32_e32 v151, v152
	v_max_f32_e32 v152, v152, v152
	v_max_f32_e32 v151, v151, v151
	v_max_f32_e32 v151, v151, v152
	v_max_f32_e32 v174, v146, v151
	v_mfma_f32_32x32x16_bf16 v[48:63], v[180:183], v[200:203], v[48:63]
	v_sub_f32_e32 v152, v151, v146
	v_sub_f32_e32 v151, v146, v174
	v_mul_f32_e32 v151, 0x3e0293ee, v151
	v_exp_f32_e32 v151, v151
	v_cmp_ge_f32_e32 vcc, s23, v152
	s_cmp_eq_u64 vcc, exec
	s_cselect_b64 s[4:5], -1, 0
	s_barrier
	s_waitcnt vmcnt(0)
	v_cndmask_b32_e64 v172, v151, 1.0, s[4:5]
	v_cmp_gt_f32_e32 vcc, 1.0, v172
	s_waitcnt vmcnt(3)
	ds_write_b128 v161, v[128:131]
	s_waitcnt vmcnt(1)
	ds_write_b128 v162, v[140:143]
	ds_write_b128 v170, v[132:135] offset:32768
	s_waitcnt vmcnt(0)
	ds_write_b128 v171, v[136:139] offset:32768
	s_cbranch_vccz .LBB0_680
	s_and_saveexec_b64 s[8:9], s[2:3]
	ds_write_b32 v157, v172 offset:128
	s_or_b64 exec, exec, s[8:9]
	s_waitcnt lgkmcnt(0)
	v_add_u32_e32 v140, v156, v148
	ds_read_b128 v[128:131], v140 offset:224
	ds_read_b128 v[132:135], v140 offset:192
	ds_read_b128 v[136:139], v140 offset:160
	ds_read_b128 v[140:143], v140 offset:128
	s_waitcnt lgkmcnt(3)
	v_pk_mul_f32 v[12:13], v[12:13], v[128:129]
	s_waitcnt lgkmcnt(2)
	v_pk_mul_f32 v[8:9], v[8:9], v[132:133]
	s_waitcnt lgkmcnt(1)
	v_pk_mul_f32 v[4:5], v[4:5], v[136:137]
	v_pk_mul_f32 v[14:15], v[14:15], v[130:131]
	v_pk_mul_f32 v[10:11], v[10:11], v[134:135]
	v_pk_mul_f32 v[6:7], v[6:7], v[138:139]
	s_waitcnt lgkmcnt(0)
	v_pk_mul_f32 v[2:3], v[2:3], v[142:143]
	v_pk_mul_f32 v[0:1], v[0:1], v[140:141]
	v_pk_mul_f32 v[28:29], v[28:29], v[128:129]
	v_pk_mul_f32 v[24:25], v[24:25], v[132:133]
	v_pk_mul_f32 v[20:21], v[20:21], v[136:137]
	v_pk_mul_f32 v[30:31], v[30:31], v[130:131]
	v_pk_mul_f32 v[26:27], v[26:27], v[134:135]
	v_pk_mul_f32 v[22:23], v[22:23], v[138:139]
	v_pk_mul_f32 v[18:19], v[18:19], v[142:143]
	v_pk_mul_f32 v[16:17], v[16:17], v[140:141]
	v_pk_mul_f32 v[44:45], v[44:45], v[128:129]
	v_pk_mul_f32 v[40:41], v[40:41], v[132:133]
	v_pk_mul_f32 v[36:37], v[36:37], v[136:137]
	v_pk_mul_f32 v[46:47], v[46:47], v[130:131]
	v_pk_mul_f32 v[42:43], v[42:43], v[134:135]
	v_pk_mul_f32 v[38:39], v[38:39], v[138:139]
	v_pk_mul_f32 v[34:35], v[34:35], v[142:143]
	v_pk_mul_f32 v[32:33], v[32:33], v[140:141]
	v_pk_mul_f32 v[60:61], v[60:61], v[128:129]
	v_pk_mul_f32 v[56:57], v[56:57], v[132:133]
	v_pk_mul_f32 v[52:53], v[52:53], v[136:137]
	v_pk_mul_f32 v[62:63], v[62:63], v[130:131]
	v_pk_mul_f32 v[58:59], v[58:59], v[134:135]
	v_pk_mul_f32 v[54:55], v[54:55], v[138:139]
	v_pk_mul_f32 v[50:51], v[50:51], v[142:143]
	v_pk_mul_f32 v[48:49], v[48:49], v[140:141]

.LBB0_1507:
	s_abs_i32 s21, s35
	s_mul_hi_u32 s22, s21, s49
	s_mul_i32 s23, s22, s48
	s_ashr_i32 s17, s35, 31
	s_sub_i32 s21, s21, s23
	s_xor_b32 s17, s17, s47
	s_add_i32 s23, s22, 1
	s_sub_i32 s24, s21, s48
	s_cmp_ge_u32 s21, s48
	s_cselect_b32 s22, s23, s22
	s_cselect_b32 s21, s24, s21
	s_add_i32 s23, s22, 1
	s_cmp_ge_u32 s21, s48
	s_cselect_b32 s21, s23, s22
	s_xor_b32 s21, s21, s17
	s_sub_i32 s17, s21, s17
	s_add_i32 s21, s19, -1
	s_min_i32 s22, s21, s46
	s_abs_i32 s24, s22
	s_mul_hi_u32 s25, s24, s49
	s_mul_i32 s26, s25, s48
	s_ashr_i32 s23, s22, 31
	s_sub_i32 s24, s24, s26
	s_xor_b32 s23, s23, s47
	s_add_i32 s26, s25, 1
	s_sub_i32 s27, s24, s48
	s_cmp_ge_u32 s24, s48
	s_cselect_b32 s25, s26, s25
	s_cselect_b32 s24, s27, s24
	s_add_i32 s26, s25, 1
	s_cmp_ge_u32 s24, s48
	s_cselect_b32 s24, s26, s25
	s_xor_b32 s24, s24, s23
	s_sub_i32 s23, s24, s23
	s_min_i32 s35, s19, s46
	s_mul_i32 s26, s23, s39
	s_mul_i32 s23, s23, s41
	s_abs_i32 s24, s35
	s_sub_i32 s22, s22, s23
	s_mul_hi_u32 s25, s24, s49
	s_mul_i32 s22, s22, s40
	s_mul_i32 s25, s25, s48
	s_add_i32 s22, s22, s37
	s_sub_i32 s24, s24, s25
	s_lshl_b32 s22, s22, 3
	s_ashr_i32 s23, s35, 31
	s_sub_i32 s25, s24, s48
	s_cmp_ge_u32 s24, s48
	s_cselect_b32 s24, s25, s24
	s_sub_i32 s25, s24, s48
	s_cmp_ge_u32 s24, s48
	s_cselect_b32 s24, s25, s24
	s_xor_b32 s24, s24, s23
	s_sub_i32 s23, s24, s23
	s_mul_i32 s23, s23, s40
	s_add_i32 s23, s23, s37
	s_mul_i32 s17, s17, s39
	s_lshl_b32 s27, s23, 3
	s_add_i32 s22, s22, s36
	s_ashr_i32 s23, s22, 31
	s_add_i32 s24, s17, s38
	s_lshl_b64 s[28:29], s[22:23], 9
	s_ashr_i32 s17, s16, 31
	ds_write_b128 v150, v[4:7]
	v_lshl_add_u64 v[4:5], v[142:143], 0, s[28:29]
	s_lshl_b64 s[28:29], s[16:17], 11
	ds_read_b128 v[80:83], v151
	s_add_u32 s25, s44, s28
	s_addc_u32 s29, s45, s29
	s_lshl_b32 s28, s24, 7
	s_ashr_i32 s30, s28, 31
	s_add_u32 s28, s25, s28
	s_addc_u32 s29, s29, s30
	s_ashr_i32 s25, s24, 31
	v_lshl_add_u64 v[72:73], s[28:29], 0, v[140:141]
	s_lshl_b64 s[28:29], s[24:25], 21
	s_waitcnt lgkmcnt(0)
	v_lshlrev_b32_e32 v76, 7, v80
	v_lshl_add_u64 v[148:149], v[144:145], 0, s[28:29]
	v_and_b32_e32 v192, 0x7fff80, v76
	v_readfirstlane_b32 s100, v148
	v_readfirstlane_b32 s101, v149
	global_load_dwordx4 v[4:7], v[4:5], off
	v_lshl_add_u64 v[76:77], v[148:149], 0, v[192:193]
	global_load_dwordx4 v[72:75], v[72:73], off
	v_mov_b32_e32 v80, v193
	global_load_dwordx4 v[136:139], v[76:77], off
	s_waitcnt vmcnt(19)
	v_dot4c_i32_i8_e32 v80, v8, v0
	v_dot4c_i32_i8_e32 v80, v9, v1
	ds_read_b128 v[84:87], v152
	ds_read_b128 v[88:91], v153
	ds_read_b128 v[76:79], v154
	v_dot4c_i32_i8_e32 v80, v10, v2
	v_dot4c_i32_i8_e32 v80, v11, v3
	s_nop 2
	v_add_u32_dpp v8, v80, v80 quad_perm:[1,0,3,2] row_mask:0xf bank_mask:0xf bound_ctrl:1
	s_nop 1
	v_add_u32_dpp v8, v8, v8 quad_perm:[2,3,0,1] row_mask:0xf bank_mask:0xf bound_ctrl:1
	s_nop 1
	v_add_u32_dpp v8, v8, v8 row_half_mirror row_mask:0xf bank_mask:0xf bound_ctrl:1
	v_cndmask_b32_e32 v10, 0, v8, vcc
	v_lshl_add_u32 v159, v81, 7, v140
	global_load_dwordx4 v[132:135], v159, s[100:101]
	v_lshl_add_u32 v159, v82, 7, v140
	global_load_dwordx4 v[128:131], v159, s[100:101]
	v_lshl_add_u32 v159, v83, 7, v140
	global_load_dwordx4 v[124:127], v159, s[100:101]
	s_waitcnt vmcnt(19)
	v_dot4_i32_i8 v155, v12, v0, 0
	v_dot4_i32_i8 v155, v13, v1, v155
	v_dot4_i32_i8 v155, v14, v2, v155
	v_dot4_i32_i8 v155, v15, v3, v155
	v_dot4_i32_i8 v156, v16, v0, 0
	v_dot4_i32_i8 v156, v17, v1, v156
	v_dot4_i32_i8 v156, v18, v2, v156
	v_dot4_i32_i8 v156, v19, v3, v156
	v_dot4_i32_i8 v157, v20, v0, 0
	v_dot4_i32_i8 v157, v21, v1, v157
	v_dot4_i32_i8 v157, v22, v2, v157
	v_dot4_i32_i8 v157, v23, v3, v157
	s_nop 0
	v_add_u32_dpp v155, v155, v155 quad_perm:[1,0,3,2] row_mask:0xf bank_mask:0xf bound_ctrl:1
	v_add_u32_dpp v156, v156, v156 quad_perm:[1,0,3,2] row_mask:0xf bank_mask:0xf bound_ctrl:1
	v_add_u32_dpp v157, v157, v157 quad_perm:[1,0,3,2] row_mask:0xf bank_mask:0xf bound_ctrl:1
	v_add_u32_dpp v155, v155, v155 quad_perm:[2,3,0,1] row_mask:0xf bank_mask:0xf bound_ctrl:1
	v_add_u32_dpp v156, v156, v156 quad_perm:[2,3,0,1] row_mask:0xf bank_mask:0xf bound_ctrl:1
	v_add_u32_dpp v157, v157, v157 quad_perm:[2,3,0,1] row_mask:0xf bank_mask:0xf bound_ctrl:1
	v_add_u32_dpp v155, v155, v155 row_half_mirror row_mask:0xf bank_mask:0xf bound_ctrl:1
	v_add_u32_dpp v156, v156, v156 row_half_mirror row_mask:0xf bank_mask:0xf bound_ctrl:1
	v_add_u32_dpp v157, v157, v157 row_half_mirror row_mask:0xf bank_mask:0xf bound_ctrl:1
	v_cndmask_b32_e64 v10, v10, v155, s[0:1]
	v_cndmask_b32_e64 v10, v10, v156, s[2:3]
	v_cndmask_b32_e64 v10, v10, v157, s[6:7]
	s_waitcnt lgkmcnt(2)
	v_lshl_add_u32 v159, v84, 7, v140
	global_load_dwordx4 v[120:123], v159, s[100:101]
	v_lshl_add_u32 v159, v85, 7, v140
	global_load_dwordx4 v[116:119], v159, s[100:101]
	v_lshl_add_u32 v159, v86, 7, v140
	global_load_dwordx4 v[112:115], v159, s[100:101]
	v_lshl_add_u32 v159, v87, 7, v140
	global_load_dwordx4 v[108:111], v159, s[100:101]
	s_waitcnt vmcnt(19)
	v_dot4_i32_i8 v155, v24, v0, 0
	v_dot4_i32_i8 v155, v25, v1, v155
	v_dot4_i32_i8 v155, v26, v2, v155
	v_dot4_i32_i8 v155, v27, v3, v155
	v_dot4_i32_i8 v156, v28, v0, 0
	v_dot4_i32_i8 v156, v29, v1, v156
	v_dot4_i32_i8 v156, v30, v2, v156
	v_dot4_i32_i8 v156, v31, v3, v156
	v_dot4_i32_i8 v157, v32, v0, 0
	v_dot4_i32_i8 v157, v33, v1, v157
	v_dot4_i32_i8 v157, v34, v2, v157
	v_dot4_i32_i8 v157, v35, v3, v157
	v_dot4_i32_i8 v158, v36, v0, 0
	v_dot4_i32_i8 v158, v37, v1, v158
	v_dot4_i32_i8 v158, v38, v2, v158
	v_dot4_i32_i8 v158, v39, v3, v158
	v_add_u32_dpp v155, v155, v155 quad_perm:[1,0,3,2] row_mask:0xf bank_mask:0xf bound_ctrl:1
	v_add_u32_dpp v156, v156, v156 quad_perm:[1,0,3,2] row_mask:0xf bank_mask:0xf bound_ctrl:1
	v_add_u32_dpp v157, v157, v157 quad_perm:[1,0,3,2] row_mask:0xf bank_mask:0xf bound_ctrl:1
	v_add_u32_dpp v158, v158, v158 quad_perm:[1,0,3,2] row_mask:0xf bank_mask:0xf bound_ctrl:1
	v_add_u32_dpp v155, v155, v155 quad_perm:[2,3,0,1] row_mask:0xf bank_mask:0xf bound_ctrl:1
	v_add_u32_dpp v156, v156, v156 quad_perm:[2,3,0,1] row_mask:0xf bank_mask:0xf bound_ctrl:1
	v_add_u32_dpp v157, v157, v157 quad_perm:[2,3,0,1] row_mask:0xf bank_mask:0xf bound_ctrl:1
	v_add_u32_dpp v158, v158, v158 quad_perm:[2,3,0,1] row_mask:0xf bank_mask:0xf bound_ctrl:1
	v_add_u32_dpp v155, v155, v155 row_half_mirror row_mask:0xf bank_mask:0xf bound_ctrl:1
	v_add_u32_dpp v156, v156, v156 row_half_mirror row_mask:0xf bank_mask:0xf bound_ctrl:1
	v_add_u32_dpp v157, v157, v157 row_half_mirror row_mask:0xf bank_mask:0xf bound_ctrl:1
	v_add_u32_dpp v158, v158, v158 row_half_mirror row_mask:0xf bank_mask:0xf bound_ctrl:1
	v_cndmask_b32_e64 v10, v10, v155, s[8:9]
	v_cndmask_b32_e64 v10, v10, v156, s[10:11]
	v_cndmask_b32_e64 v10, v10, v157, s[12:13]
	v_cndmask_b32_e64 v10, v10, v158, s[14:15]
	s_waitcnt lgkmcnt(1)
	v_lshl_add_u32 v159, v88, 7, v140
	global_load_dwordx4 v[104:107], v159, s[100:101]
	v_lshl_add_u32 v159, v89, 7, v140
	global_load_dwordx4 v[100:103], v159, s[100:101]
	v_lshl_add_u32 v159, v90, 7, v140
	global_load_dwordx4 v[96:99], v159, s[100:101]
	v_lshl_add_u32 v159, v91, 7, v140
	global_load_dwordx4 v[92:95], v159, s[100:101]
	s_waitcnt vmcnt(19)
	v_dot4_i32_i8 v155, v40, v0, 0
	v_dot4_i32_i8 v155, v41, v1, v155
	v_dot4_i32_i8 v155, v42, v2, v155
	v_dot4_i32_i8 v155, v43, v3, v155
	v_dot4_i32_i8 v156, v44, v0, 0
	v_dot4_i32_i8 v156, v45, v1, v156
	v_dot4_i32_i8 v156, v46, v2, v156
	v_dot4_i32_i8 v156, v47, v3, v156
	v_dot4_i32_i8 v157, v48, v0, 0
	v_dot4_i32_i8 v157, v49, v1, v157
	v_dot4_i32_i8 v157, v50, v2, v157
	v_dot4_i32_i8 v157, v51, v3, v157
	v_dot4_i32_i8 v158, v52, v0, 0
	v_dot4_i32_i8 v158, v53, v1, v158
	v_dot4_i32_i8 v158, v54, v2, v158
	v_dot4_i32_i8 v158, v55, v3, v158
	v_add_u32_dpp v155, v155, v155 quad_perm:[1,0,3,2] row_mask:0xf bank_mask:0xf bound_ctrl:1
	v_add_u32_dpp v156, v156, v156 quad_perm:[1,0,3,2] row_mask:0xf bank_mask:0xf bound_ctrl:1
	v_add_u32_dpp v157, v157, v157 quad_perm:[1,0,3,2] row_mask:0xf bank_mask:0xf bound_ctrl:1
	v_add_u32_dpp v158, v158, v158 quad_perm:[1,0,3,2] row_mask:0xf bank_mask:0xf bound_ctrl:1
	v_add_u32_dpp v155, v155, v155 quad_perm:[2,3,0,1] row_mask:0xf bank_mask:0xf bound_ctrl:1
	v_add_u32_dpp v156, v156, v156 quad_perm:[2,3,0,1] row_mask:0xf bank_mask:0xf bound_ctrl:1
	v_add_u32_dpp v157, v157, v157 quad_perm:[2,3,0,1] row_mask:0xf bank_mask:0xf bound_ctrl:1
	v_add_u32_dpp v158, v158, v158 quad_perm:[2,3,0,1] row_mask:0xf bank_mask:0xf bound_ctrl:1
	v_add_u32_dpp v155, v155, v155 row_half_mirror row_mask:0xf bank_mask:0xf bound_ctrl:1
	v_add_u32_dpp v156, v156, v156 row_half_mirror row_mask:0xf bank_mask:0xf bound_ctrl:1
	v_add_u32_dpp v157, v157, v157 row_half_mirror row_mask:0xf bank_mask:0xf bound_ctrl:1
	v_add_u32_dpp v158, v158, v158 row_half_mirror row_mask:0xf bank_mask:0xf bound_ctrl:1
	v_cndmask_b32_e32 v11, 0, v155, vcc
	v_cndmask_b32_e64 v11, v11, v156, s[0:1]
	v_cndmask_b32_e64 v11, v11, v157, s[2:3]
	v_cndmask_b32_e64 v11, v11, v158, s[6:7]
	s_waitcnt lgkmcnt(0)
	v_lshl_add_u32 v159, v76, 7, v140
	global_load_dwordx4 v[88:91], v159, s[100:101]
	v_lshl_add_u32 v159, v77, 7, v140
	global_load_dwordx4 v[84:87], v159, s[100:101]
	v_lshl_add_u32 v159, v78, 7, v140
	global_load_dwordx4 v[80:83], v159, s[100:101]
	v_lshl_add_u32 v159, v79, 7, v140
	global_load_dwordx4 v[76:79], v159, s[100:101]
	s_waitcnt vmcnt(19)
	v_dot4_i32_i8 v155, v56, v0, 0
	v_dot4_i32_i8 v155, v57, v1, v155
	v_dot4_i32_i8 v155, v58, v2, v155
	v_dot4_i32_i8 v155, v59, v3, v155
	v_dot4_i32_i8 v156, v60, v0, 0
	v_dot4_i32_i8 v156, v61, v1, v156
	v_dot4_i32_i8 v156, v62, v2, v156
	v_dot4_i32_i8 v156, v63, v3, v156
	v_dot4_i32_i8 v157, v64, v0, 0
	v_dot4_i32_i8 v157, v65, v1, v157
	v_dot4_i32_i8 v157, v66, v2, v157
	v_dot4_i32_i8 v157, v67, v3, v157
	v_dot4_i32_i8 v158, v68, v0, 0
	v_dot4_i32_i8 v158, v69, v1, v158
	v_dot4_i32_i8 v158, v70, v2, v158
	v_dot4_i32_i8 v158, v71, v3, v158
	v_add_u32_dpp v155, v155, v155 quad_perm:[1,0,3,2] row_mask:0xf bank_mask:0xf bound_ctrl:1
	v_add_u32_dpp v156, v156, v156 quad_perm:[1,0,3,2] row_mask:0xf bank_mask:0xf bound_ctrl:1
	v_add_u32_dpp v157, v157, v157 quad_perm:[1,0,3,2] row_mask:0xf bank_mask:0xf bound_ctrl:1
	v_add_u32_dpp v158, v158, v158 quad_perm:[1,0,3,2] row_mask:0xf bank_mask:0xf bound_ctrl:1
	v_add_u32_dpp v155, v155, v155 quad_perm:[2,3,0,1] row_mask:0xf bank_mask:0xf bound_ctrl:1
	v_add_u32_dpp v156, v156, v156 quad_perm:[2,3,0,1] row_mask:0xf bank_mask:0xf bound_ctrl:1
	v_add_u32_dpp v157, v157, v157 quad_perm:[2,3,0,1] row_mask:0xf bank_mask:0xf bound_ctrl:1
	v_add_u32_dpp v158, v158, v158 quad_perm:[2,3,0,1] row_mask:0xf bank_mask:0xf bound_ctrl:1
	v_add_u32_dpp v155, v155, v155 row_half_mirror row_mask:0xf bank_mask:0xf bound_ctrl:1
	v_add_u32_dpp v156, v156, v156 row_half_mirror row_mask:0xf bank_mask:0xf bound_ctrl:1
	v_add_u32_dpp v157, v157, v157 row_half_mirror row_mask:0xf bank_mask:0xf bound_ctrl:1
	v_add_u32_dpp v158, v158, v158 row_half_mirror row_mask:0xf bank_mask:0xf bound_ctrl:1
	v_cndmask_b32_e64 v11, v11, v155, s[8:9]
	v_cndmask_b32_e64 v11, v11, v156, s[10:11]
	v_cndmask_b32_e64 v11, v11, v157, s[12:13]
	v_cndmask_b32_e64 v0, v11, v158, s[14:15]
	s_add_i32 s26, s26, s38
	s_mul_hi_i32 s25, s20, s42
	s_mul_i32 s20, s20, s42
	s_ashr_i32 s29, s18, 31
	s_add_u32 s28, s20, s18
	v_add_u32_e32 v1, 32, v10
	s_addc_u32 s29, s25, s29
	v_lshrrev_b32_e32 v1, 6, v1
	v_lshl_add_u32 v0, v0, 10, v194
	s_lshl_b64 s[28:29], s[28:29], 8
	v_bfi_b32 v2, s34, v0, v1
	v_lshl_add_u64 v[0:1], v[146:147], 0, s[28:29]
	global_store_dword v[0:1], v2, off
	s_waitcnt vmcnt(17)
	s_add_i32 s28, s27, s36
	s_ashr_i32 s29, s28, 31
	s_lshl_b64 s[30:31], s[28:29], 9
	ds_write_b128 v150, v[4:7]
	v_lshl_add_u64 v[0:1], v[142:143], 0, s[30:31]
	s_lshl_b64 s[30:31], s[22:23], 11
	ds_read_b128 v[18:21], v151
	s_add_u32 s18, s44, s30
	s_addc_u32 s20, s45, s31
	s_lshl_b32 s23, s26, 7
	s_ashr_i32 s25, s23, 31
	s_add_u32 s30, s18, s23
	s_addc_u32 s31, s20, s25
	s_ashr_i32 s27, s26, 31
	global_load_dwordx4 v[4:7], v[0:1], off
	v_lshl_add_u64 v[0:1], s[30:31], 0, v[140:141]
	s_lshl_b64 s[30:31], s[26:27], 21
	s_waitcnt lgkmcnt(0)
	v_lshlrev_b32_e32 v8, 7, v18
	v_lshl_add_u64 v[70:71], v[144:145], 0, s[30:31]
	v_and_b32_e32 v192, 0x7fff80, v8
	v_readfirstlane_b32 s100, v70
	v_readfirstlane_b32 s101, v71
	v_lshl_add_u64 v[8:9], v[70:71], 0, v[192:193]
	global_load_dwordx4 v[0:3], v[0:1], off
	v_mov_b32_e32 v12, v193
	global_load_dwordx4 v[8:11], v[8:9], off
	s_waitcnt vmcnt(19)
	v_dot4c_i32_i8_e32 v12, v136, v72
	v_dot4c_i32_i8_e32 v12, v137, v73
	ds_read_b128 v[34:37], v152
	ds_read_b128 v[50:53], v153
	ds_read_b128 v[66:69], v154
	v_dot4c_i32_i8_e32 v12, v138, v74
	v_dot4c_i32_i8_e32 v12, v139, v75
	s_nop 2
	v_add_u32_dpp v12, v12, v12 quad_perm:[1,0,3,2] row_mask:0xf bank_mask:0xf bound_ctrl:1
	s_nop 1
	v_add_u32_dpp v12, v12, v12 quad_perm:[2,3,0,1] row_mask:0xf bank_mask:0xf bound_ctrl:1
	s_nop 1
	v_add_u32_dpp v12, v12, v12 row_half_mirror row_mask:0xf bank_mask:0xf bound_ctrl:1
	v_cndmask_b32_e32 v160, 0, v12, vcc
	v_lshl_add_u32 v159, v19, 7, v140
	global_load_dwordx4 v[12:15], v159, s[100:101]
	v_lshl_add_u32 v159, v20, 7, v140
	global_load_dwordx4 v[16:19], v159, s[100:101]
	v_lshl_add_u32 v159, v21, 7, v140
	global_load_dwordx4 v[20:23], v159, s[100:101]
	s_waitcnt vmcnt(19)
	v_dot4_i32_i8 v155, v132, v72, 0
	v_dot4_i32_i8 v155, v133, v73, v155
	v_dot4_i32_i8 v155, v134, v74, v155
	v_dot4_i32_i8 v155, v135, v75, v155
	v_dot4_i32_i8 v156, v128, v72, 0
	v_dot4_i32_i8 v156, v129, v73, v156
	v_dot4_i32_i8 v156, v130, v74, v156
	v_dot4_i32_i8 v156, v131, v75, v156
	v_dot4_i32_i8 v157, v124, v72, 0
	v_dot4_i32_i8 v157, v125, v73, v157
	v_dot4_i32_i8 v157, v126, v74, v157
	v_dot4_i32_i8 v157, v127, v75, v157
	s_nop 0
	v_add_u32_dpp v155, v155, v155 quad_perm:[1,0,3,2] row_mask:0xf bank_mask:0xf bound_ctrl:1
	v_add_u32_dpp v156, v156, v156 quad_perm:[1,0,3,2] row_mask:0xf bank_mask:0xf bound_ctrl:1
	v_add_u32_dpp v157, v157, v157 quad_perm:[1,0,3,2] row_mask:0xf bank_mask:0xf bound_ctrl:1
	v_add_u32_dpp v155, v155, v155 quad_perm:[2,3,0,1] row_mask:0xf bank_mask:0xf bound_ctrl:1
	v_add_u32_dpp v156, v156, v156 quad_perm:[2,3,0,1] row_mask:0xf bank_mask:0xf bound_ctrl:1
	v_add_u32_dpp v157, v157, v157 quad_perm:[2,3,0,1] row_mask:0xf bank_mask:0xf bound_ctrl:1
	v_add_u32_dpp v155, v155, v155 row_half_mirror row_mask:0xf bank_mask:0xf bound_ctrl:1
	v_add_u32_dpp v156, v156, v156 row_half_mirror row_mask:0xf bank_mask:0xf bound_ctrl:1
	v_add_u32_dpp v157, v157, v157 row_half_mirror row_mask:0xf bank_mask:0xf bound_ctrl:1
	v_cndmask_b32_e64 v160, v160, v155, s[0:1]
	v_cndmask_b32_e64 v160, v160, v156, s[2:3]
	v_cndmask_b32_e64 v160, v160, v157, s[6:7]
	s_waitcnt lgkmcnt(2)
	v_lshl_add_u32 v159, v34, 7, v140
	global_load_dwordx4 v[24:27], v159, s[100:101]
	v_lshl_add_u32 v159, v35, 7, v140
	global_load_dwordx4 v[28:31], v159, s[100:101]
	v_lshl_add_u32 v159, v36, 7, v140
	global_load_dwordx4 v[32:35], v159, s[100:101]
	v_lshl_add_u32 v159, v37, 7, v140
	global_load_dwordx4 v[36:39], v159, s[100:101]
	s_waitcnt vmcnt(19)
	v_dot4_i32_i8 v155, v120, v72, 0
	v_dot4_i32_i8 v155, v121, v73, v155
	v_dot4_i32_i8 v155, v122, v74, v155
	v_dot4_i32_i8 v155, v123, v75, v155
	v_dot4_i32_i8 v156, v116, v72, 0
	v_dot4_i32_i8 v156, v117, v73, v156
	v_dot4_i32_i8 v156, v118, v74, v156
	v_dot4_i32_i8 v156, v119, v75, v156
	v_dot4_i32_i8 v157, v112, v72, 0
	v_dot4_i32_i8 v157, v113, v73, v157
	v_dot4_i32_i8 v157, v114, v74, v157
	v_dot4_i32_i8 v157, v115, v75, v157
	v_dot4_i32_i8 v158, v108, v72, 0
	v_dot4_i32_i8 v158, v109, v73, v158
	v_dot4_i32_i8 v158, v110, v74, v158
	v_dot4_i32_i8 v158, v111, v75, v158
	v_add_u32_dpp v155, v155, v155 quad_perm:[1,0,3,2] row_mask:0xf bank_mask:0xf bound_ctrl:1
	v_add_u32_dpp v156, v156, v156 quad_perm:[1,0,3,2] row_mask:0xf bank_mask:0xf bound_ctrl:1
	v_add_u32_dpp v157, v157, v157 quad_perm:[1,0,3,2] row_mask:0xf bank_mask:0xf bound_ctrl:1
	v_add_u32_dpp v158, v158, v158 quad_perm:[1,0,3,2] row_mask:0xf bank_mask:0xf bound_ctrl:1
	v_add_u32_dpp v155, v155, v155 quad_perm:[2,3,0,1] row_mask:0xf bank_mask:0xf bound_ctrl:1
	v_add_u32_dpp v156, v156, v156 quad_perm:[2,3,0,1] row_mask:0xf bank_mask:0xf bound_ctrl:1
	v_add_u32_dpp v157, v157, v157 quad_perm:[2,3,0,1] row_mask:0xf bank_mask:0xf bound_ctrl:1
	v_add_u32_dpp v158, v158, v158 quad_perm:[2,3,0,1] row_mask:0xf bank_mask:0xf bound_ctrl:1
	v_add_u32_dpp v155, v155, v155 row_half_mirror row_mask:0xf bank_mask:0xf bound_ctrl:1
	v_add_u32_dpp v156, v156, v156 row_half_mirror row_mask:0xf bank_mask:0xf bound_ctrl:1
	v_add_u32_dpp v157, v157, v157 row_half_mirror row_mask:0xf bank_mask:0xf bound_ctrl:1
	v_add_u32_dpp v158, v158, v158 row_half_mirror row_mask:0xf bank_mask:0xf bound_ctrl:1
	v_cndmask_b32_e64 v160, v160, v155, s[8:9]
	v_cndmask_b32_e64 v160, v160, v156, s[10:11]
	v_cndmask_b32_e64 v160, v160, v157, s[12:13]
	v_cndmask_b32_e64 v160, v160, v158, s[14:15]
	s_waitcnt lgkmcnt(1)
	v_lshl_add_u32 v159, v50, 7, v140
	global_load_dwordx4 v[40:43], v159, s[100:101]
	v_lshl_add_u32 v159, v51, 7, v140
	global_load_dwordx4 v[44:47], v159, s[100:101]
	v_lshl_add_u32 v159, v52, 7, v140
	global_load_dwordx4 v[48:51], v159, s[100:101]
	v_lshl_add_u32 v159, v53, 7, v140
	global_load_dwordx4 v[52:55], v159, s[100:101]
	s_waitcnt vmcnt(19)
	v_dot4_i32_i8 v155, v104, v72, 0
	v_dot4_i32_i8 v155, v105, v73, v155
	v_dot4_i32_i8 v155, v106, v74, v155
	v_dot4_i32_i8 v155, v107, v75, v155
	v_dot4_i32_i8 v156, v100, v72, 0
	v_dot4_i32_i8 v156, v101, v73, v156
	v_dot4_i32_i8 v156, v102, v74, v156
	v_dot4_i32_i8 v156, v103, v75, v156
	v_dot4_i32_i8 v157, v96, v72, 0
	v_dot4_i32_i8 v157, v97, v73, v157
	v_dot4_i32_i8 v157, v98, v74, v157
	v_dot4_i32_i8 v157, v99, v75, v157
	v_dot4_i32_i8 v158, v92, v72, 0
	v_dot4_i32_i8 v158, v93, v73, v158
	v_dot4_i32_i8 v158, v94, v74, v158
	v_dot4_i32_i8 v158, v95, v75, v158
	v_add_u32_dpp v155, v155, v155 quad_perm:[1,0,3,2] row_mask:0xf bank_mask:0xf bound_ctrl:1
	v_add_u32_dpp v156, v156, v156 quad_perm:[1,0,3,2] row_mask:0xf bank_mask:0xf bound_ctrl:1
	v_add_u32_dpp v157, v157, v157 quad_perm:[1,0,3,2] row_mask:0xf bank_mask:0xf bound_ctrl:1
	v_add_u32_dpp v158, v158, v158 quad_perm:[1,0,3,2] row_mask:0xf bank_mask:0xf bound_ctrl:1
	v_add_u32_dpp v155, v155, v155 quad_perm:[2,3,0,1] row_mask:0xf bank_mask:0xf bound_ctrl:1
	v_add_u32_dpp v156, v156, v156 quad_perm:[2,3,0,1] row_mask:0xf bank_mask:0xf bound_ctrl:1
	v_add_u32_dpp v157, v157, v157 quad_perm:[2,3,0,1] row_mask:0xf bank_mask:0xf bound_ctrl:1
	v_add_u32_dpp v158, v158, v158 quad_perm:[2,3,0,1] row_mask:0xf bank_mask:0xf bound_ctrl:1
	v_add_u32_dpp v155, v155, v155 row_half_mirror row_mask:0xf bank_mask:0xf bound_ctrl:1
	v_add_u32_dpp v156, v156, v156 row_half_mirror row_mask:0xf bank_mask:0xf bound_ctrl:1
	v_add_u32_dpp v157, v157, v157 row_half_mirror row_mask:0xf bank_mask:0xf bound_ctrl:1
	v_add_u32_dpp v158, v158, v158 row_half_mirror row_mask:0xf bank_mask:0xf bound_ctrl:1
	v_cndmask_b32_e32 v161, 0, v155, vcc
	v_cndmask_b32_e64 v161, v161, v156, s[0:1]
	v_cndmask_b32_e64 v161, v161, v157, s[2:3]
	v_cndmask_b32_e64 v161, v161, v158, s[6:7]
	s_waitcnt lgkmcnt(0)
	v_lshl_add_u32 v159, v66, 7, v140
	global_load_dwordx4 v[56:59], v159, s[100:101]
	v_lshl_add_u32 v159, v67, 7, v140
	global_load_dwordx4 v[60:63], v159, s[100:101]
	v_lshl_add_u32 v159, v68, 7, v140
	global_load_dwordx4 v[64:67], v159, s[100:101]
	v_lshl_add_u32 v159, v69, 7, v140
	global_load_dwordx4 v[68:71], v159, s[100:101]
	s_waitcnt vmcnt(19)
	v_dot4_i32_i8 v155, v88, v72, 0
	v_dot4_i32_i8 v155, v89, v73, v155
	v_dot4_i32_i8 v155, v90, v74, v155
	v_dot4_i32_i8 v155, v91, v75, v155
	v_dot4_i32_i8 v156, v84, v72, 0
	v_dot4_i32_i8 v156, v85, v73, v156
	v_dot4_i32_i8 v156, v86, v74, v156
	v_dot4_i32_i8 v156, v87, v75, v156
	v_dot4_i32_i8 v157, v80, v72, 0
	v_dot4_i32_i8 v157, v81, v73, v157
	v_dot4_i32_i8 v157, v82, v74, v157
	v_dot4_i32_i8 v157, v83, v75, v157
	v_dot4_i32_i8 v158, v76, v72, 0
	v_dot4_i32_i8 v158, v77, v73, v158
	v_dot4_i32_i8 v158, v78, v74, v158
	v_dot4_i32_i8 v158, v79, v75, v158
	v_add_u32_dpp v155, v155, v155 quad_perm:[1,0,3,2] row_mask:0xf bank_mask:0xf bound_ctrl:1
	v_add_u32_dpp v156, v156, v156 quad_perm:[1,0,3,2] row_mask:0xf bank_mask:0xf bound_ctrl:1
	v_add_u32_dpp v157, v157, v157 quad_perm:[1,0,3,2] row_mask:0xf bank_mask:0xf bound_ctrl:1
	v_add_u32_dpp v158, v158, v158 quad_perm:[1,0,3,2] row_mask:0xf bank_mask:0xf bound_ctrl:1
	v_add_u32_dpp v155, v155, v155 quad_perm:[2,3,0,1] row_mask:0xf bank_mask:0xf bound_ctrl:1
	v_add_u32_dpp v156, v156, v156 quad_perm:[2,3,0,1] row_mask:0xf bank_mask:0xf bound_ctrl:1
	v_add_u32_dpp v157, v157, v157 quad_perm:[2,3,0,1] row_mask:0xf bank_mask:0xf bound_ctrl:1
	v_add_u32_dpp v158, v158, v158 quad_perm:[2,3,0,1] row_mask:0xf bank_mask:0xf bound_ctrl:1
	v_add_u32_dpp v155, v155, v155 row_half_mirror row_mask:0xf bank_mask:0xf bound_ctrl:1
	v_add_u32_dpp v156, v156, v156 row_half_mirror row_mask:0xf bank_mask:0xf bound_ctrl:1
	v_add_u32_dpp v157, v157, v157 row_half_mirror row_mask:0xf bank_mask:0xf bound_ctrl:1
	v_add_u32_dpp v158, v158, v158 row_half_mirror row_mask:0xf bank_mask:0xf bound_ctrl:1
	v_cndmask_b32_e64 v161, v161, v155, s[8:9]
	v_cndmask_b32_e64 v161, v161, v156, s[10:11]
	v_cndmask_b32_e64 v161, v161, v157, s[12:13]
	v_cndmask_b32_e64 v161, v161, v158, s[14:15]
	v_mov_b32_e32 v108, v160
	v_mov_b32_e32 v72, v161
	s_mul_i32 s20, s24, s42
	s_mul_hi_i32 s18, s24, s42
	s_add_u32 s16, s20, s16
	v_add_u32_e32 v73, 32, v108
	s_addc_u32 s17, s18, s17
	v_lshrrev_b32_e32 v73, 6, v73
	v_lshl_add_u32 v72, v72, 10, v194
	s_lshl_b64 s[16:17], s[16:17], 8
	v_bfi_b32 v74, s34, v72, v73
	v_lshl_add_u64 v[72:73], v[146:147], 0, s[16:17]
	global_store_dword v[72:73], v74, off
	s_waitcnt vmcnt(17)
	s_add_i32 s19, s19, 2
	s_cmp_lt_i32 s21, s43
	s_mov_b32 s18, s22
	s_mov_b32 s20, s26
	s_mov_b32 s16, s28
	s_cbranch_scc1 .LBB0_1507
